# on top of v44: leading wave group defers its K-loop vmcnt wait from before the pre-MMA barrier to before the post-MMA barrier (one more barrier interval of LDS-DMA latency tolerance)
# speedup vs baseline: 1.0012x; 1.0012x over previous
; #define PG8_STAGE(bufoff, gbase, voff) do { _Pragma("unroll") for (int _i = 0; _i < 2; ++_i) \
;         __builtin_amdgcn_global_load_lds((const unsigned*)((const char*)(gbase) + (voff)[_i]), (LAS unsigned*)(lds + (bufoff) + ldsw + _i * 8192), 16, 0, 0); } while (0)
; #define PG8_LDA(dst, b, h) do { if constexpr (FP8) { _Pragma("unroll") for (int m = 0; m < 4; ++m) dst##8[m] = PG8_LD8(lds + PG8_SA(b, h) + aoff + m * 2048); } \
;         else { _Pragma("unroll") for (int m = 0; m < 4; ++m) _Pragma("unroll") for (int k = 0; k < 2; ++k) dst[m][k] = *(const LAS bf16x8*)(lds + PG8_SA(b, h) + aoff + m * 2048 + k * 1024); } } while (0)
; #define PG8_LDB(dst, b, h) do { if constexpr (FP8) { _Pragma("unroll") for (int n = 0; n < 2; ++n) dst##8[n] = PG8_LD8(lds + PG8_SB(b, h) + boff + n * 2048); } \
;         else { _Pragma("unroll") for (int n = 0; n < 2; ++n) _Pragma("unroll") for (int k = 0; k < 2; ++k) dst[n][k] = *(const LAS bf16x8*)(lds + PG8_SB(b, h) + boff + n * 2048 + k * 1024); } } while (0)
; #define PG8_WAIT_V(n) asm volatile("s_waitcnt vmcnt(" #n ")" ::: "memory")
; #define PG8_WAIT_L(n) asm volatile("s_waitcnt lgkmcnt(" #n ")" ::: "memory")
; #define PG8_BAR __builtin_amdgcn_s_barrier()
; #define PG8_SCHED __builtin_amdgcn_sched_barrier(0)
; template <class Epi, class Sched, bool ALIGN_EPI, bool SP2, bool FP8 = false>
; __device__ __forceinline__ void gemm_phase(LAS unsigned char* lds, const int K, const Sched& S, const Epi& E) {
;     ...
;         for (int t = 0; t < nt; t += 2) {
;             const bool last = (t == nt - 2);
;             const char* a1 = cA + (size_t)(t + 1) * kstep;
;             const char* a2 = last ? nA : cA + (size_t)(t + 2) * kstep; const char* b2 = last ? nB : cB + (size_t)(t + 2) * kstep;
;             const char* a3 = a2 + kstep; const char* b3 = b2 + kstep;
;             unsigned vX0[2], vX1[2];
; #pragma unroll
;             for (int i = 0; i < 2; ++i) { vX0[i] = last ? vAn[0][i] : vAc[0][i]; vX1[i] = last ? vAn[1][i] : vAc[1][i]; }
;             PG8_LDB(B0, 0, 0); PG8_LDB(B1, 0, 1); PG8_SCHED; PG8_LDA(At, 0, 0); PG8_STAGE(PG8_SA(1, 1), a1, vAc[1]);
;             PG8_WAIT_V(8); PG8_WAIT_L(0); PG8_BAR; PG8_MMA(0, 0, At, B0); PG8_MMA(0, 1, At, B1); PG8_BAR; PG8_SCHED;
;             PG8_LDA(At, 0, 1); PG8_STAGE(PG8_SB(0, 0), b2, voffB); PG8_STAGE(PG8_SB(0, 1), b2 + hstep, voffB); PG8_STAGE(PG8_SA(0, 0), a2, vX0);
.LBB0_203:
	s_add_u32 s70, s4, s68
	s_addc_u32 s71, s5, s69
	v_add_u32_e32 v145, s87, v167
	s_add_u32 s72, s70, 0x100
	ds_read_b128 v[154:157], v183
	ds_read_b128 v[158:161], v183 offset:1024
	ds_read_b128 v[192:195], v183 offset:2048
	ds_read_b128 v[196:199], v183 offset:3072
	ds_read_b128 v[200:203], v145
	ds_read_b128 v[204:207], v145 offset:1024
	ds_read_b128 v[208:211], v145 offset:2048
	ds_read_b128 v[212:215], v145 offset:3072
	s_addc_u32 s73, s71, 0
	s_add_u32 s82, s45, s68
	s_addc_u32 s83, s96, s69
	s_cmpk_eq_i32 s68, 0xf00
	s_cselect_b64 vcc, -1, 0
	s_and_b64 s[70:71], vcc, exec
	v_cndmask_b32_e32 v136, v144, v186, vcc
	s_cselect_b32 s73, s63, s73
	s_cselect_b32 s72, s62, s72
	v_cndmask_b32_e32 v143, v142, v187, vcc
	v_cndmask_b32_e32 v162, v148, v188, vcc
	v_cndmask_b32_e32 v145, v146, v189, vcc
	s_cselect_b32 s71, s65, s83
	s_cselect_b32 s70, s64, s82
	v_lshl_add_u64 v[248:249], v[152:153], 0, s[68:69]
	s_add_i32 m0, s67, 0xc000
	ds_read_b128 v[216:219], v184
	ds_read_b128 v[220:223], v184 offset:1024
	ds_read_b128 v[224:227], v184 offset:2048
	ds_read_b128 v[228:231], v184 offset:3072
	ds_read_b128 v[232:235], v184 offset:4096
	ds_read_b128 v[236:239], v184 offset:5120
	ds_read_b128 v[240:243], v184 offset:6144
	ds_read_b128 v[244:247], v184 offset:7168
	global_load_lds_dwordx4 v[248:249], off
	v_lshl_add_u64 v[248:249], v[150:151], 0, s[68:69]
	s_add_i32 m0, s67, 0xe000
	s_nop 0
	global_load_lds_dwordx4 v[248:249], off
	s_bitcmp1_b32 s58, 0
	s_cbranch_scc1 .Lg0skip_1
	s_waitcnt vmcnt(8)
.Lg0skip_1:
	s_waitcnt lgkmcnt(0)
	s_setprio 1
	s_barrier
	v_mfma_f32_16x16x32_bf16 v[62:65], v[154:157], v[216:219], v[62:65]
	v_mfma_f32_16x16x32_bf16 v[58:61], v[192:195], v[216:219], v[58:61]
	v_mfma_f32_16x16x32_bf16 v[54:57], v[154:157], v[224:227], v[54:57]
	v_mfma_f32_16x16x32_bf16 v[50:53], v[192:195], v[224:227], v[50:53]
	v_mfma_f32_16x16x32_bf16 v[46:49], v[154:157], v[232:235], v[46:49]
	v_mfma_f32_16x16x32_bf16 v[42:45], v[192:195], v[232:235], v[42:45]
	v_mfma_f32_16x16x32_bf16 v[38:41], v[154:157], v[240:243], v[38:41]
	v_mfma_f32_16x16x32_bf16 v[34:37], v[192:195], v[240:243], v[34:37]
	v_mfma_f32_16x16x32_bf16 v[62:65], v[158:161], v[220:223], v[62:65]
	v_mfma_f32_16x16x32_bf16 v[58:61], v[196:199], v[220:223], v[58:61]
	v_mfma_f32_16x16x32_bf16 v[54:57], v[158:161], v[228:231], v[54:57]
	v_mfma_f32_16x16x32_bf16 v[50:53], v[196:199], v[228:231], v[50:53]
	v_mfma_f32_16x16x32_bf16 v[46:49], v[158:161], v[236:239], v[46:49]
	v_mfma_f32_16x16x32_bf16 v[42:45], v[196:199], v[236:239], v[42:45]
	v_mfma_f32_16x16x32_bf16 v[38:41], v[158:161], v[244:247], v[38:41]
	v_mfma_f32_16x16x32_bf16 v[34:37], v[196:199], v[244:247], v[34:37]
	v_mfma_f32_16x16x32_bf16 v[126:129], v[200:203], v[216:219], v[126:129]
	v_mfma_f32_16x16x32_bf16 v[122:125], v[208:211], v[216:219], v[122:125]
	v_mfma_f32_16x16x32_bf16 v[118:121], v[200:203], v[224:227], v[118:121]
	v_mfma_f32_16x16x32_bf16 v[114:117], v[208:211], v[224:227], v[114:117]
	v_mfma_f32_16x16x32_bf16 v[110:113], v[200:203], v[232:235], v[110:113]
	v_mfma_f32_16x16x32_bf16 v[106:109], v[208:211], v[232:235], v[106:109]
	v_mfma_f32_16x16x32_bf16 v[102:105], v[200:203], v[240:243], v[102:105]
	v_mfma_f32_16x16x32_bf16 v[98:101], v[208:211], v[240:243], v[98:101]
	v_mfma_f32_16x16x32_bf16 v[126:129], v[204:207], v[220:223], v[126:129]
	v_mfma_f32_16x16x32_bf16 v[122:125], v[212:215], v[220:223], v[122:125]
	v_mfma_f32_16x16x32_bf16 v[118:121], v[204:207], v[228:231], v[118:121]
	v_mfma_f32_16x16x32_bf16 v[114:117], v[212:215], v[228:231], v[114:117]
	v_mfma_f32_16x16x32_bf16 v[110:113], v[204:207], v[236:239], v[110:113]
	v_mfma_f32_16x16x32_bf16 v[106:109], v[212:215], v[236:239], v[106:109]
	v_mfma_f32_16x16x32_bf16 v[102:105], v[204:207], v[244:247], v[102:105]
	v_mfma_f32_16x16x32_bf16 v[98:101], v[212:215], v[244:247], v[98:101]
	s_setprio 0
	s_waitcnt vmcnt(8)
	s_barrier
	s_add_i32 s82, s86, s74
	v_lshl_add_u64 v[248:249], s[70:71], 0, v[132:133]
	s_mov_b32 m0, s82
	ds_read_b128 v[216:219], v184 offset:16384
	ds_read_b128 v[220:223], v184 offset:17408
	ds_read_b128 v[224:227], v184 offset:18432
	ds_read_b128 v[228:231], v184 offset:19456
	ds_read_b128 v[232:235], v184 offset:20480
	ds_read_b128 v[236:239], v184 offset:21504
	ds_read_b128 v[240:243], v184 offset:22528
	ds_read_b128 v[244:247], v184 offset:23552
	global_load_lds_dwordx4 v[248:249], off
	s_add_i32 m0, s82, 0x2000
	s_add_u32 vcc_lo, s70, 0x80000
	v_lshl_add_u64 v[250:251], s[70:71], 0, v[134:135]
	s_addc_u32 vcc_hi, s71, 0
	s_add_i32 s82, s87, s74
	global_load_lds_dwordx4 v[250:251], off
	v_lshl_add_u64 v[252:253], vcc, 0, v[132:133]
	s_mov_b32 m0, s82
	v_mov_b32_e32 v163, v137
	global_load_lds_dwordx4 v[252:253], off
	v_lshl_add_u64 v[252:253], vcc, 0, v[134:135]
	s_add_i32 m0, s82, 0x2000
	s_nop 0
	global_load_lds_dwordx4 v[252:253], off
	s_mov_b32 m0, s67
	v_lshl_add_u64 v[252:253], s[72:73], 0, v[136:137]
	global_load_lds_dwordx4 v136, s[72:73]
	s_mov_b32 m0, s75
	s_nop 0
	global_load_lds_dwordx4 v162, s[72:73]
	s_bitcmp1_b32 s58, 0
	s_cbranch_scc1 .Lg0skip_2
	s_waitcnt vmcnt(8)
; #define PG8_STAGE(bufoff, gbase, voff) do { _Pragma("unroll") for (int _i = 0; _i < 2; ++_i) \
;         __builtin_amdgcn_global_load_lds((const unsigned*)((const char*)(gbase) + (voff)[_i]), (LAS unsigned*)(lds + (bufoff) + ldsw + _i * 8192), 16, 0, 0); } while (0)
; #define PG8_LDA(dst, b, h) do { if constexpr (FP8) { _Pragma("unroll") for (int m = 0; m < 4; ++m) dst##8[m] = PG8_LD8(lds + PG8_SA(b, h) + aoff + m * 2048); } \
;         else { _Pragma("unroll") for (int m = 0; m < 4; ++m) _Pragma("unroll") for (int k = 0; k < 2; ++k) dst[m][k] = *(const LAS bf16x8*)(lds + PG8_SA(b, h) + aoff + m * 2048 + k * 1024); } } while (0)
; #define PG8_LDB(dst, b, h) do { if constexpr (FP8) { _Pragma("unroll") for (int n = 0; n < 2; ++n) dst##8[n] = PG8_LD8(lds + PG8_SB(b, h) + boff + n * 2048); } \
;         else { _Pragma("unroll") for (int n = 0; n < 2; ++n) _Pragma("unroll") for (int k = 0; k < 2; ++k) dst[n][k] = *(const LAS bf16x8*)(lds + PG8_SB(b, h) + boff + n * 2048 + k * 1024); } } while (0)
; #define PG8_WAIT_V(n) asm volatile("s_waitcnt vmcnt(" #n ")" ::: "memory")
; #define PG8_WAIT_L(n) asm volatile("s_waitcnt lgkmcnt(" #n ")" ::: "memory")
; #define PG8_BAR __builtin_amdgcn_s_barrier()
; #define PG8_SCHED __builtin_amdgcn_sched_barrier(0)
; template <class Epi, class Sched, bool ALIGN_EPI, bool SP2, bool FP8 = false>
; __device__ __forceinline__ void gemm_phase(LAS unsigned char* lds, const int K, const Sched& S, const Epi& E) {
;     ...
;             PG8_WAIT_V(8); PG8_WAIT_L(0); PG8_BAR; PG8_MMA(1, 0, At, B0); PG8_MMA(1, 1, At, B1); PG8_BAR; PG8_SCHED;
;             PG8_LDB(B0, 1, 0); PG8_LDB(B1, 1, 1); PG8_SCHED; PG8_LDA(At, 1, 0); PG8_STAGE(PG8_SA(0, 1), a2, vX1);
.Lg0skip_2:
	s_waitcnt lgkmcnt(0)
	v_lshl_add_u64 v[162:163], s[72:73], 0, v[162:163]
	s_setprio 1
	s_barrier
	v_mfma_f32_16x16x32_bf16 v[30:33], v[154:157], v[216:219], v[30:33]
	v_mfma_f32_16x16x32_bf16 v[26:29], v[192:195], v[216:219], v[26:29]
	v_mfma_f32_16x16x32_bf16 v[22:25], v[154:157], v[224:227], v[22:25]
	v_mfma_f32_16x16x32_bf16 v[18:21], v[192:195], v[224:227], v[18:21]
	v_mfma_f32_16x16x32_bf16 v[14:17], v[154:157], v[232:235], v[14:17]
	v_mfma_f32_16x16x32_bf16 v[10:13], v[192:195], v[232:235], v[10:13]
	v_mfma_f32_16x16x32_bf16 v[6:9], v[154:157], v[240:243], v[6:9]
	v_mfma_f32_16x16x32_bf16 v[2:5], v[192:195], v[240:243], v[2:5]
	v_mfma_f32_16x16x32_bf16 v[30:33], v[158:161], v[220:223], v[30:33]
	v_mfma_f32_16x16x32_bf16 v[26:29], v[196:199], v[220:223], v[26:29]
	v_mfma_f32_16x16x32_bf16 v[22:25], v[158:161], v[228:231], v[22:25]
	v_mfma_f32_16x16x32_bf16 v[18:21], v[196:199], v[228:231], v[18:21]
	v_mfma_f32_16x16x32_bf16 v[14:17], v[158:161], v[236:239], v[14:17]
	v_mfma_f32_16x16x32_bf16 v[10:13], v[196:199], v[236:239], v[10:13]
	v_mfma_f32_16x16x32_bf16 v[6:9], v[158:161], v[244:247], v[6:9]
	v_mfma_f32_16x16x32_bf16 v[2:5], v[196:199], v[244:247], v[2:5]
	v_mfma_f32_16x16x32_bf16 v[94:97], v[200:203], v[216:219], v[94:97]
	v_mfma_f32_16x16x32_bf16 v[90:93], v[208:211], v[216:219], v[90:93]
	v_mfma_f32_16x16x32_bf16 v[86:89], v[200:203], v[224:227], v[86:89]
	v_mfma_f32_16x16x32_bf16 v[82:85], v[208:211], v[224:227], v[82:85]
	v_mfma_f32_16x16x32_bf16 v[78:81], v[200:203], v[232:235], v[78:81]
	v_mfma_f32_16x16x32_bf16 v[74:77], v[208:211], v[232:235], v[74:77]
	v_mfma_f32_16x16x32_bf16 v[66:69], v[200:203], v[240:243], v[66:69]
	v_mfma_f32_16x16x32_bf16 v[70:73], v[208:211], v[240:243], v[70:73]
	v_mfma_f32_16x16x32_bf16 v[94:97], v[204:207], v[220:223], v[94:97]
	v_mfma_f32_16x16x32_bf16 v[90:93], v[212:215], v[220:223], v[90:93]
	v_mfma_f32_16x16x32_bf16 v[86:89], v[204:207], v[228:231], v[86:89]
	v_mfma_f32_16x16x32_bf16 v[82:85], v[212:215], v[228:231], v[82:85]
	v_mfma_f32_16x16x32_bf16 v[78:81], v[204:207], v[236:239], v[78:81]
	v_mfma_f32_16x16x32_bf16 v[74:77], v[212:215], v[236:239], v[74:77]
	v_mfma_f32_16x16x32_bf16 v[66:69], v[204:207], v[244:247], v[66:69]
	v_mfma_f32_16x16x32_bf16 v[70:73], v[212:215], v[244:247], v[70:73]
	s_setprio 0
	s_waitcnt vmcnt(8)
	s_barrier
	s_add_i32 s82, 0, 0x18000
	v_add_u32_e32 v136, s82, v167
	s_add_i32 s83, 0, 0x1c000
	ds_read_b128 v[154:157], v136
	ds_read_b128 v[158:161], v136 offset:1024
	ds_read_b128 v[192:195], v136 offset:2048
	ds_read_b128 v[196:199], v136 offset:3072
	v_add_u32_e32 v136, s83, v167
	ds_read_b128 v[200:203], v136
	ds_read_b128 v[204:207], v136 offset:1024
	ds_read_b128 v[208:211], v136 offset:2048
	ds_read_b128 v[212:215], v136 offset:3072
	s_mov_b32 m0, s76
	ds_read_b128 v[216:219], v184 offset:32768
	ds_read_b128 v[220:223], v184 offset:33792
	ds_read_b128 v[224:227], v184 offset:34816
	ds_read_b128 v[228:231], v184 offset:35840
	ds_read_b128 v[232:235], v184 offset:36864
	ds_read_b128 v[236:239], v184 offset:37888
	ds_read_b128 v[240:243], v184 offset:38912
	ds_read_b128 v[244:247], v184 offset:39936
	global_load_lds_dwordx4 v143, s[72:73]
	s_mov_b32 m0, s77
	s_nop 0
	global_load_lds_dwordx4 v145, s[72:73]
	s_bitcmp1_b32 s58, 0
	s_cbranch_scc1 .Lg0skip_3
	s_waitcnt vmcnt(8)
; #define PG8_STAGE(bufoff, gbase, voff) do { _Pragma("unroll") for (int _i = 0; _i < 2; ++_i) \
;         __builtin_amdgcn_global_load_lds((const unsigned*)((const char*)(gbase) + (voff)[_i]), (LAS unsigned*)(lds + (bufoff) + ldsw + _i * 8192), 16, 0, 0); } while (0)
; #define PG8_LDA(dst, b, h) do { if constexpr (FP8) { _Pragma("unroll") for (int m = 0; m < 4; ++m) dst##8[m] = PG8_LD8(lds + PG8_SA(b, h) + aoff + m * 2048); } \
;         else { _Pragma("unroll") for (int m = 0; m < 4; ++m) _Pragma("unroll") for (int k = 0; k < 2; ++k) dst[m][k] = *(const LAS bf16x8*)(lds + PG8_SA(b, h) + aoff + m * 2048 + k * 1024); } } while (0)
; #define PG8_WAIT_V(n) asm volatile("s_waitcnt vmcnt(" #n ")" ::: "memory")
; #define PG8_WAIT_L(n) asm volatile("s_waitcnt lgkmcnt(" #n ")" ::: "memory")
; #define PG8_BAR __builtin_amdgcn_s_barrier()
; #define PG8_SCHED __builtin_amdgcn_sched_barrier(0)
; template <class Epi, class Sched, bool ALIGN_EPI, bool SP2, bool FP8 = false>
; __device__ __forceinline__ void gemm_phase(LAS unsigned char* lds, const int K, const Sched& S, const Epi& E) {
;     ...
;             PG8_WAIT_V(8); PG8_WAIT_L(0); PG8_BAR; PG8_MMA(0, 0, At, B0); PG8_MMA(0, 1, At, B1); PG8_BAR; PG8_SCHED;
;             PG8_LDA(At, 1, 1); PG8_STAGE(PG8_SB(1, 0), b3, voffB); PG8_STAGE(PG8_SB(1, 1), b3 + hstep, voffB); PG8_STAGE(PG8_SA(1, 0), a3, vX0);
;             PG8_WAIT_V(8); PG8_WAIT_L(0); PG8_BAR; PG8_MMA(1, 0, At, B0); PG8_MMA(1, 1, At, B1); PG8_BAR; PG8_SCHED;
;         }
;         if constexpr (ALIGN_EPI) { if (wr == 0) PG8_BAR; }
.Lg0skip_3:
	s_waitcnt lgkmcnt(0)
	s_setprio 1
	s_barrier
	v_mfma_f32_16x16x32_bf16 v[62:65], v[154:157], v[216:219], v[62:65]
	v_mfma_f32_16x16x32_bf16 v[58:61], v[192:195], v[216:219], v[58:61]
	v_mfma_f32_16x16x32_bf16 v[54:57], v[154:157], v[224:227], v[54:57]
	v_mfma_f32_16x16x32_bf16 v[50:53], v[192:195], v[224:227], v[50:53]
	v_mfma_f32_16x16x32_bf16 v[46:49], v[154:157], v[232:235], v[46:49]
	v_mfma_f32_16x16x32_bf16 v[42:45], v[192:195], v[232:235], v[42:45]
	v_mfma_f32_16x16x32_bf16 v[38:41], v[154:157], v[240:243], v[38:41]
	v_mfma_f32_16x16x32_bf16 v[34:37], v[192:195], v[240:243], v[34:37]
	v_mfma_f32_16x16x32_bf16 v[62:65], v[158:161], v[220:223], v[62:65]
	v_mfma_f32_16x16x32_bf16 v[58:61], v[196:199], v[220:223], v[58:61]
	v_mfma_f32_16x16x32_bf16 v[54:57], v[158:161], v[228:231], v[54:57]
	v_mfma_f32_16x16x32_bf16 v[50:53], v[196:199], v[228:231], v[50:53]
	v_mfma_f32_16x16x32_bf16 v[46:49], v[158:161], v[236:239], v[46:49]
	v_mfma_f32_16x16x32_bf16 v[42:45], v[196:199], v[236:239], v[42:45]
	v_mfma_f32_16x16x32_bf16 v[38:41], v[158:161], v[244:247], v[38:41]
	v_mfma_f32_16x16x32_bf16 v[34:37], v[196:199], v[244:247], v[34:37]
	v_mfma_f32_16x16x32_bf16 v[126:129], v[200:203], v[216:219], v[126:129]
	v_mfma_f32_16x16x32_bf16 v[122:125], v[208:211], v[216:219], v[122:125]
	v_mfma_f32_16x16x32_bf16 v[118:121], v[200:203], v[224:227], v[118:121]
	v_mfma_f32_16x16x32_bf16 v[114:117], v[208:211], v[224:227], v[114:117]
	v_mfma_f32_16x16x32_bf16 v[110:113], v[200:203], v[232:235], v[110:113]
	v_mfma_f32_16x16x32_bf16 v[106:109], v[208:211], v[232:235], v[106:109]
	v_mfma_f32_16x16x32_bf16 v[102:105], v[200:203], v[240:243], v[102:105]
	v_mfma_f32_16x16x32_bf16 v[98:101], v[208:211], v[240:243], v[98:101]
	v_mfma_f32_16x16x32_bf16 v[126:129], v[204:207], v[220:223], v[126:129]
	v_mfma_f32_16x16x32_bf16 v[122:125], v[212:215], v[220:223], v[122:125]
	v_mfma_f32_16x16x32_bf16 v[118:121], v[204:207], v[228:231], v[118:121]
	v_mfma_f32_16x16x32_bf16 v[114:117], v[212:215], v[228:231], v[114:117]
	v_mfma_f32_16x16x32_bf16 v[110:113], v[204:207], v[236:239], v[110:113]
	v_mfma_f32_16x16x32_bf16 v[106:109], v[212:215], v[236:239], v[106:109]
	v_mfma_f32_16x16x32_bf16 v[102:105], v[204:207], v[244:247], v[102:105]
	v_mfma_f32_16x16x32_bf16 v[98:101], v[212:215], v[244:247], v[98:101]
	s_setprio 0
	s_waitcnt vmcnt(8)
	s_barrier
	s_add_i32 s72, s82, s74
	v_lshl_add_u64 v[248:249], v[248:249], 0, s[50:51]
	s_mov_b32 m0, s72
	ds_read_b128 v[216:219], v184 offset:49152
	ds_read_b128 v[220:223], v184 offset:50176
	ds_read_b128 v[224:227], v184 offset:51200
	ds_read_b128 v[228:231], v184 offset:52224
	ds_read_b128 v[232:235], v184 offset:53248
	ds_read_b128 v[236:239], v184 offset:54272
	ds_read_b128 v[240:243], v184 offset:55296
	ds_read_b128 v[244:247], v184 offset:56320
	global_load_lds_dwordx4 v[248:249], off
	s_add_i32 m0, s72, 0x2000
	s_add_u32 s70, s70, 0x80080
	v_lshl_add_u64 v[248:249], v[250:251], 0, s[50:51]
	s_addc_u32 s71, s71, 0
	s_add_i32 s72, s83, s74
	global_load_lds_dwordx4 v[248:249], off
	v_lshl_add_u64 v[248:249], s[70:71], 0, v[132:133]
	s_mov_b32 m0, s72
	v_lshl_add_u64 v[162:163], v[162:163], 0, s[50:51]
	global_load_lds_dwordx4 v[248:249], off
	v_lshl_add_u64 v[248:249], s[70:71], 0, v[134:135]
	s_add_i32 m0, s72, 0x2000
	s_nop 0
	global_load_lds_dwordx4 v[248:249], off
	v_lshl_add_u64 v[248:249], v[252:253], 0, s[50:51]
	s_mov_b32 m0, s79
	s_nop 0
	global_load_lds_dwordx4 v[248:249], off
	s_mov_b32 m0, s80
	s_nop 0
	global_load_lds_dwordx4 v[162:163], off
	s_bitcmp1_b32 s58, 0
	s_cbranch_scc1 .Lg0skip_4
	s_waitcnt vmcnt(8)
.Lg0skip_4:
	s_waitcnt lgkmcnt(0)
	s_setprio 1
	s_barrier
	v_mfma_f32_16x16x32_bf16 v[30:33], v[154:157], v[216:219], v[30:33]
	v_mfma_f32_16x16x32_bf16 v[26:29], v[192:195], v[216:219], v[26:29]
	v_mfma_f32_16x16x32_bf16 v[22:25], v[154:157], v[224:227], v[22:25]
	v_mfma_f32_16x16x32_bf16 v[18:21], v[192:195], v[224:227], v[18:21]
	v_mfma_f32_16x16x32_bf16 v[14:17], v[154:157], v[232:235], v[14:17]
	v_mfma_f32_16x16x32_bf16 v[10:13], v[192:195], v[232:235], v[10:13]
	v_mfma_f32_16x16x32_bf16 v[6:9], v[154:157], v[240:243], v[6:9]
	v_mfma_f32_16x16x32_bf16 v[2:5], v[192:195], v[240:243], v[2:5]
	v_mfma_f32_16x16x32_bf16 v[30:33], v[158:161], v[220:223], v[30:33]
	v_mfma_f32_16x16x32_bf16 v[26:29], v[196:199], v[220:223], v[26:29]
	v_mfma_f32_16x16x32_bf16 v[22:25], v[158:161], v[228:231], v[22:25]
	v_mfma_f32_16x16x32_bf16 v[18:21], v[196:199], v[228:231], v[18:21]
	v_mfma_f32_16x16x32_bf16 v[14:17], v[158:161], v[236:239], v[14:17]
	v_mfma_f32_16x16x32_bf16 v[10:13], v[196:199], v[236:239], v[10:13]
	v_mfma_f32_16x16x32_bf16 v[6:9], v[158:161], v[244:247], v[6:9]
	v_mfma_f32_16x16x32_bf16 v[2:5], v[196:199], v[244:247], v[2:5]
	v_mfma_f32_16x16x32_bf16 v[94:97], v[200:203], v[216:219], v[94:97]
	v_mfma_f32_16x16x32_bf16 v[90:93], v[208:211], v[216:219], v[90:93]
	v_mfma_f32_16x16x32_bf16 v[86:89], v[200:203], v[224:227], v[86:89]
	v_mfma_f32_16x16x32_bf16 v[82:85], v[208:211], v[224:227], v[82:85]
	v_mfma_f32_16x16x32_bf16 v[78:81], v[200:203], v[232:235], v[78:81]
	v_mfma_f32_16x16x32_bf16 v[74:77], v[208:211], v[232:235], v[74:77]
	v_mfma_f32_16x16x32_bf16 v[66:69], v[200:203], v[240:243], v[66:69]
	v_mfma_f32_16x16x32_bf16 v[70:73], v[208:211], v[240:243], v[70:73]
	v_mfma_f32_16x16x32_bf16 v[94:97], v[204:207], v[220:223], v[94:97]
	v_mfma_f32_16x16x32_bf16 v[90:93], v[212:215], v[220:223], v[90:93]
	v_mfma_f32_16x16x32_bf16 v[86:89], v[204:207], v[228:231], v[86:89]
	v_mfma_f32_16x16x32_bf16 v[82:85], v[212:215], v[228:231], v[82:85]
	v_mfma_f32_16x16x32_bf16 v[78:81], v[204:207], v[236:239], v[78:81]
	v_mfma_f32_16x16x32_bf16 v[74:77], v[212:215], v[236:239], v[74:77]
	v_mfma_f32_16x16x32_bf16 v[66:69], v[204:207], v[244:247], v[66:69]
	v_mfma_f32_16x16x32_bf16 v[70:73], v[212:215], v[244:247], v[70:73]
	s_setprio 0
	s_waitcnt vmcnt(8)
	s_barrier
	s_add_i32 s97, s97, 2
	s_add_u32 s68, s68, 0x100
	s_addc_u32 s69, s69, 0
	s_cmp_gt_u32 s97, 29
	s_cbranch_scc0 .LBB0_203
	s_and_b64 vcc, exec, s[58:59]
	s_cbranch_vccz .LBB0_206
	s_barrier

; #define PG8_STAGE(bufoff, gbase, voff) do { _Pragma("unroll") for (int _i = 0; _i < 2; ++_i) \
;         __builtin_amdgcn_global_load_lds((const unsigned*)((const char*)(gbase) + (voff)[_i]), (LAS unsigned*)(lds + (bufoff) + ldsw + _i * 8192), 16, 0, 0); } while (0)
; #define PG8_LDA(dst, b, h) do { if constexpr (FP8) { _Pragma("unroll") for (int m = 0; m < 4; ++m) dst##8[m] = PG8_LD8(lds + PG8_SA(b, h) + aoff + m * 2048); } \
;         else { _Pragma("unroll") for (int m = 0; m < 4; ++m) _Pragma("unroll") for (int k = 0; k < 2; ++k) dst[m][k] = *(const LAS bf16x8*)(lds + PG8_SA(b, h) + aoff + m * 2048 + k * 1024); } } while (0)
; #define PG8_LDB(dst, b, h) do { if constexpr (FP8) { _Pragma("unroll") for (int n = 0; n < 2; ++n) dst##8[n] = PG8_LD8(lds + PG8_SB(b, h) + boff + n * 2048); } \
;         else { _Pragma("unroll") for (int n = 0; n < 2; ++n) _Pragma("unroll") for (int k = 0; k < 2; ++k) dst[n][k] = *(const LAS bf16x8*)(lds + PG8_SB(b, h) + boff + n * 2048 + k * 1024); } } while (0)
; #define PG8_WAIT_V(n) asm volatile("s_waitcnt vmcnt(" #n ")" ::: "memory")
; #define PG8_WAIT_L(n) asm volatile("s_waitcnt lgkmcnt(" #n ")" ::: "memory")
; #define PG8_BAR __builtin_amdgcn_s_barrier()
; #define PG8_SCHED __builtin_amdgcn_sched_barrier(0)
; template <class Epi, class Sched, bool ALIGN_EPI, bool SP2, bool FP8 = false>
; __device__ __forceinline__ void gemm_phase(LAS unsigned char* lds, const int K, const Sched& S, const Epi& E) {
;     ...
;         for (int t = 0; t < nt; t += 2) {
;             const bool last = (t == nt - 2);
;             const char* a1 = cA + (size_t)(t + 1) * kstep;
;             const char* a2 = last ? nA : cA + (size_t)(t + 2) * kstep; const char* b2 = last ? nB : cB + (size_t)(t + 2) * kstep;
;             const char* a3 = a2 + kstep; const char* b3 = b2 + kstep;
;             unsigned vX0[2], vX1[2];
; #pragma unroll
;             for (int i = 0; i < 2; ++i) { vX0[i] = last ? vAn[0][i] : vAc[0][i]; vX1[i] = last ? vAn[1][i] : vAc[1][i]; }
;             PG8_LDB(B0, 0, 0); PG8_LDB(B1, 0, 1); PG8_SCHED; PG8_LDA(At, 0, 0); PG8_STAGE(PG8_SA(1, 1), a1, vAc[1]);
;             PG8_WAIT_V(8); PG8_WAIT_L(0); PG8_BAR; PG8_MMA(0, 0, At, B0); PG8_MMA(0, 1, At, B1); PG8_BAR; PG8_SCHED;
;             PG8_LDA(At, 0, 1); PG8_STAGE(PG8_SB(0, 0), b2, voffB); PG8_STAGE(PG8_SB(0, 1), b2 + hstep, voffB); PG8_STAGE(PG8_SA(0, 0), a2, vX0);
.LBB0_790:
	ds_read_b128 v[18:21], v191
	ds_read_b128 v[22:25], v191 offset:1024
	ds_read_b128 v[26:29], v191 offset:2048
	ds_read_b128 v[30:33], v191 offset:3072
	ds_read_b128 v[2:5], v192
	ds_read_b128 v[6:9], v192 offset:1024
	ds_read_b128 v[10:13], v192 offset:2048
	ds_read_b128 v[14:17], v192 offset:3072
	s_add_u32 s60, s30, s58
	s_addc_u32 s61, s31, s59
	s_add_u32 s62, s60, 0x12000100
	s_addc_u32 s63, s61, 0
	s_add_u32 s72, s49, s58
	s_addc_u32 s73, s57, s59
	s_cmpk_eq_i32 s58, 0x700
	s_cselect_b64 vcc, -1, 0
	s_and_b64 s[60:61], vcc, exec
	v_cndmask_b32_e32 v166, v173, v195, vcc
	s_cselect_b32 s63, s9, s63
	s_cselect_b32 s62, s8, s62
	v_cndmask_b32_e32 v169, v168, v196, vcc
	v_cndmask_b32_e32 v232, v172, v197, vcc
	v_cndmask_b32_e32 v171, v170, v198, vcc
	s_cselect_b32 s61, s51, s73
	s_cselect_b32 s60, s50, s72
	v_lshl_add_u64 v[224:225], v[176:177], 0, s[58:59]
	s_add_i32 m0, s47, 0xc000
	ds_read_b128 v[178:181], v193
	ds_read_b128 v[182:185], v193 offset:1024
	ds_read_b128 v[200:203], v193 offset:2048
	ds_read_b128 v[204:207], v193 offset:3072
	ds_read_b128 v[208:211], v193 offset:4096
	ds_read_b128 v[212:215], v193 offset:5120
	ds_read_b128 v[216:219], v193 offset:6144
	ds_read_b128 v[220:223], v193 offset:7168
	global_load_lds_dwordx4 v[224:225], off
	v_lshl_add_u64 v[224:225], v[174:175], 0, s[58:59]
	s_add_i32 m0, s47, 0xe000
	s_nop 0
	global_load_lds_dwordx4 v[224:225], off
	s_bitcmp1_b32 s44, 0
	s_cbranch_scc1 .Lg0skip_5
	s_waitcnt vmcnt(8)
.Lg0skip_5:
	s_waitcnt lgkmcnt(0)
	s_setprio 1
	s_barrier
	v_mfma_f32_16x16x128_f8f6f4 v[158:161], v[18:25], v[178:185], v[158:161]
	v_mfma_f32_16x16x128_f8f6f4 v[154:157], v[26:33], v[178:185], v[154:157]
	v_mfma_f32_16x16x128_f8f6f4 v[142:145], v[18:25], v[200:207], v[142:145]
	v_mfma_f32_16x16x128_f8f6f4 v[138:141], v[26:33], v[200:207], v[138:141]
	v_mfma_f32_16x16x128_f8f6f4 v[126:129], v[18:25], v[208:215], v[126:129]
	v_mfma_f32_16x16x128_f8f6f4 v[122:125], v[26:33], v[208:215], v[122:125]
	v_mfma_f32_16x16x128_f8f6f4 v[110:113], v[18:25], v[216:223], v[110:113]
	v_mfma_f32_16x16x128_f8f6f4 v[106:109], v[26:33], v[216:223], v[106:109]
	v_mfma_f32_16x16x128_f8f6f4 v[150:153], v[2:9], v[178:185], v[150:153]
	v_mfma_f32_16x16x128_f8f6f4 v[146:149], v[10:17], v[178:185], v[146:149]
	v_mfma_f32_16x16x128_f8f6f4 v[134:137], v[2:9], v[200:207], v[134:137]
	v_mfma_f32_16x16x128_f8f6f4 v[130:133], v[10:17], v[200:207], v[130:133]
	v_mfma_f32_16x16x128_f8f6f4 v[118:121], v[2:9], v[208:215], v[118:121]
	v_mfma_f32_16x16x128_f8f6f4 v[114:117], v[10:17], v[208:215], v[114:117]
	v_mfma_f32_16x16x128_f8f6f4 v[102:105], v[2:9], v[216:223], v[102:105]
	v_mfma_f32_16x16x128_f8f6f4 v[98:101], v[10:17], v[216:223], v[98:101]
	s_setprio 0
	s_waitcnt vmcnt(8)
	s_barrier
	s_add_i32 s72, s67, s35
	v_lshl_add_u64 v[178:179], s[60:61], 0, v[162:163]
	s_mov_b32 m0, s72
	ds_read_b128 v[200:203], v193 offset:16384
	ds_read_b128 v[204:207], v193 offset:17408
	ds_read_b128 v[208:211], v193 offset:18432
	ds_read_b128 v[212:215], v193 offset:19456
	ds_read_b128 v[216:219], v193 offset:20480
	ds_read_b128 v[220:223], v193 offset:21504
	ds_read_b128 v[224:227], v193 offset:22528
	ds_read_b128 v[228:231], v193 offset:23552
	global_load_lds_dwordx4 v[178:179], off
	s_add_i32 m0, s72, 0x2000
	s_add_u32 s72, s60, 0x40000
	v_lshl_add_u64 v[180:181], s[60:61], 0, v[164:165]
	s_addc_u32 s73, s61, 0
	s_add_i32 s74, s68, s35
	global_load_lds_dwordx4 v[180:181], off
	v_lshl_add_u64 v[182:183], s[72:73], 0, v[162:163]
	s_mov_b32 m0, s74
	v_mov_b32_e32 v233, v167
	global_load_lds_dwordx4 v[182:183], off
	v_lshl_add_u64 v[182:183], s[72:73], 0, v[164:165]
	s_add_i32 m0, s74, 0x2000
	v_lshl_add_u64 v[184:185], s[62:63], 0, v[166:167]
	global_load_lds_dwordx4 v[182:183], off
	s_mov_b32 m0, s47
	v_lshl_add_u64 v[182:183], s[62:63], 0, v[232:233]
	global_load_lds_dwordx4 v166, s[62:63]
	s_mov_b32 m0, s53
	s_nop 0
	global_load_lds_dwordx4 v232, s[62:63]
	s_bitcmp1_b32 s44, 0
	s_cbranch_scc1 .Lg0skip_6
	s_waitcnt vmcnt(8)
; #define PG8_STAGE(bufoff, gbase, voff) do { _Pragma("unroll") for (int _i = 0; _i < 2; ++_i) \
;         __builtin_amdgcn_global_load_lds((const unsigned*)((const char*)(gbase) + (voff)[_i]), (LAS unsigned*)(lds + (bufoff) + ldsw + _i * 8192), 16, 0, 0); } while (0)
; #define PG8_LDA(dst, b, h) do { if constexpr (FP8) { _Pragma("unroll") for (int m = 0; m < 4; ++m) dst##8[m] = PG8_LD8(lds + PG8_SA(b, h) + aoff + m * 2048); } \
;         else { _Pragma("unroll") for (int m = 0; m < 4; ++m) _Pragma("unroll") for (int k = 0; k < 2; ++k) dst[m][k] = *(const LAS bf16x8*)(lds + PG8_SA(b, h) + aoff + m * 2048 + k * 1024); } } while (0)
; #define PG8_LDB(dst, b, h) do { if constexpr (FP8) { _Pragma("unroll") for (int n = 0; n < 2; ++n) dst##8[n] = PG8_LD8(lds + PG8_SB(b, h) + boff + n * 2048); } \
;         else { _Pragma("unroll") for (int n = 0; n < 2; ++n) _Pragma("unroll") for (int k = 0; k < 2; ++k) dst[n][k] = *(const LAS bf16x8*)(lds + PG8_SB(b, h) + boff + n * 2048 + k * 1024); } } while (0)
; #define PG8_WAIT_V(n) asm volatile("s_waitcnt vmcnt(" #n ")" ::: "memory")
; #define PG8_WAIT_L(n) asm volatile("s_waitcnt lgkmcnt(" #n ")" ::: "memory")
; #define PG8_BAR __builtin_amdgcn_s_barrier()
; #define PG8_SCHED __builtin_amdgcn_sched_barrier(0)
; template <class Epi, class Sched, bool ALIGN_EPI, bool SP2, bool FP8 = false>
; __device__ __forceinline__ void gemm_phase(LAS unsigned char* lds, const int K, const Sched& S, const Epi& E) {
;     ...
;             PG8_WAIT_V(8); PG8_WAIT_L(0); PG8_BAR; PG8_MMA(1, 0, At, B0); PG8_MMA(1, 1, At, B1); PG8_BAR; PG8_SCHED;
;             PG8_LDB(B0, 1, 0); PG8_LDB(B1, 1, 1); PG8_SCHED; PG8_LDA(At, 1, 0); PG8_STAGE(PG8_SA(0, 1), a2, vX1);
;             PG8_WAIT_V(8); PG8_WAIT_L(0); PG8_BAR; PG8_MMA(0, 0, At, B0); PG8_MMA(0, 1, At, B1); PG8_BAR; PG8_SCHED;
;             PG8_LDA(At, 1, 1); PG8_STAGE(PG8_SB(1, 0), b3, voffB); PG8_STAGE(PG8_SB(1, 1), b3 + hstep, voffB); PG8_STAGE(PG8_SA(1, 0), a3, vX0);
;             PG8_WAIT_V(8); PG8_WAIT_L(0); PG8_BAR; PG8_MMA(1, 0, At, B0); PG8_MMA(1, 1, At, B1); PG8_BAR; PG8_SCHED;
;         }
;         if constexpr (ALIGN_EPI) { if (wr == 0) PG8_BAR; }
.Lg0skip_6:
	s_waitcnt lgkmcnt(0)
	s_setprio 1
	s_barrier
	v_mfma_f32_16x16x128_f8f6f4 v[94:97], v[18:25], v[200:207], v[94:97]
	v_mfma_f32_16x16x128_f8f6f4 v[90:93], v[26:33], v[200:207], v[90:93]
	v_mfma_f32_16x16x128_f8f6f4 v[78:81], v[18:25], v[208:215], v[78:81]
	v_mfma_f32_16x16x128_f8f6f4 v[74:77], v[26:33], v[208:215], v[74:77]
	v_mfma_f32_16x16x128_f8f6f4 v[54:57], v[18:25], v[216:223], v[54:57]
	v_mfma_f32_16x16x128_f8f6f4 v[50:53], v[26:33], v[216:223], v[50:53]
	v_mfma_f32_16x16x128_f8f6f4 v[38:41], v[18:25], v[224:231], v[38:41]
	v_mfma_f32_16x16x128_f8f6f4 v[34:37], v[26:33], v[224:231], v[34:37]
	v_mfma_f32_16x16x128_f8f6f4 v[86:89], v[2:9], v[200:207], v[86:89]
	v_mfma_f32_16x16x128_f8f6f4 v[82:85], v[10:17], v[200:207], v[82:85]
	v_mfma_f32_16x16x128_f8f6f4 v[70:73], v[2:9], v[208:215], v[70:73]
	v_mfma_f32_16x16x128_f8f6f4 v[66:69], v[10:17], v[208:215], v[66:69]
	v_mfma_f32_16x16x128_f8f6f4 v[62:65], v[2:9], v[216:223], v[62:65]
	v_mfma_f32_16x16x128_f8f6f4 v[58:61], v[10:17], v[216:223], v[58:61]
	v_mfma_f32_16x16x128_f8f6f4 v[46:49], v[2:9], v[224:231], v[46:49]
	v_mfma_f32_16x16x128_f8f6f4 v[42:45], v[10:17], v[224:231], v[42:45]
	s_setprio 0
	s_waitcnt vmcnt(8)
	s_barrier
	s_add_i32 s72, 0, 0x18000
	s_add_i32 s73, 0, 0x1c000
	v_add_u32_e32 v14, s72, v188
	v_add_u32_e32 v30, s73, v188
	ds_read_b128 v[2:5], v14
	ds_read_b128 v[6:9], v14 offset:1024
	ds_read_b128 v[10:13], v14 offset:2048
	ds_read_b128 v[14:17], v14 offset:3072
	ds_read_b128 v[18:21], v30
	ds_read_b128 v[22:25], v30 offset:1024
	ds_read_b128 v[26:29], v30 offset:2048
	ds_read_b128 v[30:33], v30 offset:3072
	s_mov_b32 m0, s54
	ds_read_b128 v[200:203], v193 offset:32768
	ds_read_b128 v[204:207], v193 offset:33792
	ds_read_b128 v[208:211], v193 offset:34816
	ds_read_b128 v[212:215], v193 offset:35840
	ds_read_b128 v[216:219], v193 offset:36864
	ds_read_b128 v[220:223], v193 offset:37888
	ds_read_b128 v[224:227], v193 offset:38912
	ds_read_b128 v[228:231], v193 offset:39936
	global_load_lds_dwordx4 v169, s[62:63]
	s_mov_b32 m0, s55
	s_nop 0
	global_load_lds_dwordx4 v171, s[62:63]
	s_bitcmp1_b32 s44, 0
	s_cbranch_scc1 .Lg0skip_7
	s_waitcnt vmcnt(8)
.Lg0skip_7:
	s_waitcnt lgkmcnt(0)
	s_setprio 1
	s_barrier
	v_mfma_f32_16x16x128_f8f6f4 v[158:161], v[2:9], v[200:207], v[158:161]
	v_mfma_f32_16x16x128_f8f6f4 v[154:157], v[10:17], v[200:207], v[154:157]
	v_mfma_f32_16x16x128_f8f6f4 v[142:145], v[2:9], v[208:215], v[142:145]
	v_mfma_f32_16x16x128_f8f6f4 v[138:141], v[10:17], v[208:215], v[138:141]
	v_mfma_f32_16x16x128_f8f6f4 v[126:129], v[2:9], v[216:223], v[126:129]
	v_mfma_f32_16x16x128_f8f6f4 v[122:125], v[10:17], v[216:223], v[122:125]
	v_mfma_f32_16x16x128_f8f6f4 v[110:113], v[2:9], v[224:231], v[110:113]
	v_mfma_f32_16x16x128_f8f6f4 v[106:109], v[10:17], v[224:231], v[106:109]
	v_mfma_f32_16x16x128_f8f6f4 v[150:153], v[18:25], v[200:207], v[150:153]
	v_mfma_f32_16x16x128_f8f6f4 v[146:149], v[26:33], v[200:207], v[146:149]
	v_mfma_f32_16x16x128_f8f6f4 v[134:137], v[18:25], v[208:215], v[134:137]
	v_mfma_f32_16x16x128_f8f6f4 v[130:133], v[26:33], v[208:215], v[130:133]
	v_mfma_f32_16x16x128_f8f6f4 v[118:121], v[18:25], v[216:223], v[118:121]
	v_mfma_f32_16x16x128_f8f6f4 v[114:117], v[26:33], v[216:223], v[114:117]
	v_mfma_f32_16x16x128_f8f6f4 v[102:105], v[18:25], v[224:231], v[102:105]
	v_mfma_f32_16x16x128_f8f6f4 v[98:101], v[26:33], v[224:231], v[98:101]
	s_setprio 0
	s_waitcnt vmcnt(8)
	s_barrier
	s_add_i32 s62, s72, s35
	v_lshl_add_u64 v[178:179], v[178:179], 0, s[40:41]
	s_mov_b32 m0, s62
	ds_read_b128 v[200:203], v193 offset:49152
	ds_read_b128 v[204:207], v193 offset:50176
	ds_read_b128 v[208:211], v193 offset:51200
	ds_read_b128 v[212:215], v193 offset:52224
	ds_read_b128 v[216:219], v193 offset:53248
	ds_read_b128 v[220:223], v193 offset:54272
	ds_read_b128 v[224:227], v193 offset:55296
	ds_read_b128 v[228:231], v193 offset:56320
	global_load_lds_dwordx4 v[178:179], off
	s_add_i32 m0, s62, 0x2000
	s_add_u32 s60, s60, 0x40080
	v_lshl_add_u64 v[178:179], v[180:181], 0, s[40:41]
	s_addc_u32 s61, s61, 0
	s_add_i32 s62, s73, s35
	global_load_lds_dwordx4 v[178:179], off
	v_lshl_add_u64 v[178:179], s[60:61], 0, v[162:163]
	s_mov_b32 m0, s62
	s_nop 0
	global_load_lds_dwordx4 v[178:179], off
	v_lshl_add_u64 v[178:179], s[60:61], 0, v[164:165]
	s_add_i32 m0, s62, 0x2000
	s_nop 0
	global_load_lds_dwordx4 v[178:179], off
	v_lshl_add_u64 v[178:179], v[184:185], 0, s[40:41]
	s_mov_b32 m0, s65
	s_nop 0
	global_load_lds_dwordx4 v[178:179], off
	v_lshl_add_u64 v[178:179], v[182:183], 0, s[40:41]
	s_mov_b32 m0, s66
	s_nop 0
	global_load_lds_dwordx4 v[178:179], off
	s_bitcmp1_b32 s44, 0
	s_cbranch_scc1 .Lg0skip_8
	s_waitcnt vmcnt(8)
.Lg0skip_8:
	s_waitcnt lgkmcnt(0)
	s_setprio 1
	s_barrier
	v_mfma_f32_16x16x128_f8f6f4 v[94:97], v[2:9], v[200:207], v[94:97]
	v_mfma_f32_16x16x128_f8f6f4 v[90:93], v[10:17], v[200:207], v[90:93]
	v_mfma_f32_16x16x128_f8f6f4 v[78:81], v[2:9], v[208:215], v[78:81]
	v_mfma_f32_16x16x128_f8f6f4 v[74:77], v[10:17], v[208:215], v[74:77]
	v_mfma_f32_16x16x128_f8f6f4 v[54:57], v[2:9], v[216:223], v[54:57]
	v_mfma_f32_16x16x128_f8f6f4 v[50:53], v[10:17], v[216:223], v[50:53]
	v_mfma_f32_16x16x128_f8f6f4 v[38:41], v[2:9], v[224:231], v[38:41]
	v_mfma_f32_16x16x128_f8f6f4 v[34:37], v[10:17], v[224:231], v[34:37]
	v_mfma_f32_16x16x128_f8f6f4 v[86:89], v[18:25], v[200:207], v[86:89]
	v_mfma_f32_16x16x128_f8f6f4 v[82:85], v[26:33], v[200:207], v[82:85]
	v_mfma_f32_16x16x128_f8f6f4 v[70:73], v[18:25], v[208:215], v[70:73]
	v_mfma_f32_16x16x128_f8f6f4 v[66:69], v[26:33], v[208:215], v[66:69]
	v_mfma_f32_16x16x128_f8f6f4 v[62:65], v[18:25], v[216:223], v[62:65]
	v_mfma_f32_16x16x128_f8f6f4 v[58:61], v[26:33], v[216:223], v[58:61]
	v_mfma_f32_16x16x128_f8f6f4 v[46:49], v[18:25], v[224:231], v[46:49]
	v_mfma_f32_16x16x128_f8f6f4 v[42:45], v[26:33], v[224:231], v[42:45]
	s_setprio 0
	s_waitcnt vmcnt(8)
	s_barrier
	s_add_i32 s71, s71, 2
	s_add_u32 s58, s58, 0x100
	s_addc_u32 s59, s59, 0
	s_cmp_gt_u32 s71, 13
	s_cbranch_scc0 .LBB0_790
	s_and_b64 vcc, exec, s[44:45]
	s_cbranch_vccz .LBB0_793
	s_barrier

; #define PG8_STAGE(bufoff, gbase, voff) do { _Pragma("unroll") for (int _i = 0; _i < 2; ++_i) \
;         __builtin_amdgcn_global_load_lds((const unsigned*)((const char*)(gbase) + (voff)[_i]), (LAS unsigned*)(lds + (bufoff) + ldsw + _i * 8192), 16, 0, 0); } while (0)
; #define PG8_LDA(dst, b, h) do { if constexpr (FP8) { _Pragma("unroll") for (int m = 0; m < 4; ++m) dst##8[m] = PG8_LD8(lds + PG8_SA(b, h) + aoff + m * 2048); } \
;         else { _Pragma("unroll") for (int m = 0; m < 4; ++m) _Pragma("unroll") for (int k = 0; k < 2; ++k) dst[m][k] = *(const LAS bf16x8*)(lds + PG8_SA(b, h) + aoff + m * 2048 + k * 1024); } } while (0)
; #define PG8_LDB(dst, b, h) do { if constexpr (FP8) { _Pragma("unroll") for (int n = 0; n < 2; ++n) dst##8[n] = PG8_LD8(lds + PG8_SB(b, h) + boff + n * 2048); } \
;         else { _Pragma("unroll") for (int n = 0; n < 2; ++n) _Pragma("unroll") for (int k = 0; k < 2; ++k) dst[n][k] = *(const LAS bf16x8*)(lds + PG8_SB(b, h) + boff + n * 2048 + k * 1024); } } while (0)
; #define PG8_WAIT_V(n) asm volatile("s_waitcnt vmcnt(" #n ")" ::: "memory")
; #define PG8_WAIT_L(n) asm volatile("s_waitcnt lgkmcnt(" #n ")" ::: "memory")
; #define PG8_BAR __builtin_amdgcn_s_barrier()
; #define PG8_SCHED __builtin_amdgcn_sched_barrier(0)
; template <class Epi, class Sched, bool ALIGN_EPI, bool SP2, bool FP8 = false>
; __device__ __forceinline__ void gemm_phase(LAS unsigned char* lds, const int K, const Sched& S, const Epi& E) {
;     ...
;         for (int t = 0; t < nt; t += 2) {
;             const bool last = (t == nt - 2);
;             const char* a1 = cA + (size_t)(t + 1) * kstep;
;             const char* a2 = last ? nA : cA + (size_t)(t + 2) * kstep; const char* b2 = last ? nB : cB + (size_t)(t + 2) * kstep;
;             const char* a3 = a2 + kstep; const char* b3 = b2 + kstep;
;             unsigned vX0[2], vX1[2];
; #pragma unroll
;             for (int i = 0; i < 2; ++i) { vX0[i] = last ? vAn[0][i] : vAc[0][i]; vX1[i] = last ? vAn[1][i] : vAc[1][i]; }
;             PG8_LDB(B0, 0, 0); PG8_LDB(B1, 0, 1); PG8_SCHED; PG8_LDA(At, 0, 0); PG8_STAGE(PG8_SA(1, 1), a1, vAc[1]);
;             PG8_WAIT_V(8); PG8_WAIT_L(0); PG8_BAR; PG8_MMA(0, 0, At, B0); PG8_MMA(0, 1, At, B1); PG8_BAR; PG8_SCHED;
;             PG8_LDA(At, 0, 1); PG8_STAGE(PG8_SB(0, 0), b2, voffB); PG8_STAGE(PG8_SB(0, 1), b2 + hstep, voffB); PG8_STAGE(PG8_SA(0, 0), a2, vX0);
.LBB0_883:
	ds_read_b128 v[162:165], v153
	ds_read_b128 v[166:169], v153 offset:1024
	ds_read_b128 v[170:173], v153 offset:2048
	ds_read_b128 v[174:177], v153 offset:3072
	ds_read_b128 v[178:181], v154
	ds_read_b128 v[182:185], v154 offset:1024
	ds_read_b128 v[186:189], v154 offset:2048
	ds_read_b128 v[192:195], v154 offset:3072
	s_add_u32 s6, s30, s4
	s_addc_u32 s7, s31, s5
	s_add_u32 s50, s6, 0x1e000100
	s_addc_u32 s51, s7, 0
	s_add_u32 s70, s47, s4
	s_addc_u32 s71, s68, s5
	s_cmpk_eq_i32 s4, 0xf00
	s_cselect_b64 vcc, -1, 0
	s_and_b64 s[6:7], vcc, exec
	v_cndmask_b32_e32 v136, v143, v158, vcc
	s_cselect_b32 s51, s15, s51
	s_cselect_b32 s50, s14, s50
	v_cndmask_b32_e32 v139, v138, v159, vcc
	v_cndmask_b32_e32 v228, v142, v160, vcc
	v_cndmask_b32_e32 v141, v140, v161, vcc
	s_cselect_b32 s7, s49, s71
	s_cselect_b32 s6, s48, s70
	s_mov_b32 m0, s64
	v_lshl_add_u64 v[230:231], v[146:147], 0, s[4:5]
	ds_read_b128 v[196:199], v155
	ds_read_b128 v[200:203], v155 offset:1024
	ds_read_b128 v[204:207], v155 offset:2048
	ds_read_b128 v[208:211], v155 offset:3072
	ds_read_b128 v[212:215], v155 offset:4096
	ds_read_b128 v[216:219], v155 offset:5120
	ds_read_b128 v[220:223], v155 offset:6144
	ds_read_b128 v[224:227], v155 offset:7168
	global_load_lds_dwordx4 v[230:231], off
	v_lshl_add_u64 v[230:231], v[144:145], 0, s[4:5]
	s_add_i32 m0, s53, 0xe000
	s_nop 0
	global_load_lds_dwordx4 v[230:231], off
	s_bitcmp1_b32 s44, 0
	s_cbranch_scc1 .Lg0skip_9
	s_waitcnt vmcnt(8)
.Lg0skip_9:
	s_waitcnt lgkmcnt(0)
	s_setprio 1
	s_barrier
	v_mfma_f32_16x16x32_bf16 v[126:129], v[162:165], v[196:199], v[126:129]
	v_mfma_f32_16x16x32_bf16 v[122:125], v[170:173], v[196:199], v[122:125]
	v_mfma_f32_16x16x32_bf16 v[118:121], v[162:165], v[204:207], v[118:121]
	v_mfma_f32_16x16x32_bf16 v[114:117], v[170:173], v[204:207], v[114:117]
	v_mfma_f32_16x16x32_bf16 v[94:97], v[162:165], v[212:215], v[94:97]
	v_mfma_f32_16x16x32_bf16 v[90:93], v[170:173], v[212:215], v[90:93]
	v_mfma_f32_16x16x32_bf16 v[78:81], v[162:165], v[220:223], v[78:81]
	v_mfma_f32_16x16x32_bf16 v[74:77], v[170:173], v[220:223], v[74:77]
	v_mfma_f32_16x16x32_bf16 v[126:129], v[166:169], v[200:203], v[126:129]
	v_mfma_f32_16x16x32_bf16 v[122:125], v[174:177], v[200:203], v[122:125]
	v_mfma_f32_16x16x32_bf16 v[118:121], v[166:169], v[208:211], v[118:121]
	v_mfma_f32_16x16x32_bf16 v[114:117], v[174:177], v[208:211], v[114:117]
	v_mfma_f32_16x16x32_bf16 v[94:97], v[166:169], v[216:219], v[94:97]
	v_mfma_f32_16x16x32_bf16 v[90:93], v[174:177], v[216:219], v[90:93]
	v_mfma_f32_16x16x32_bf16 v[78:81], v[166:169], v[224:227], v[78:81]
	v_mfma_f32_16x16x32_bf16 v[74:77], v[174:177], v[224:227], v[74:77]
	v_mfma_f32_16x16x32_bf16 v[110:113], v[178:181], v[196:199], v[110:113]
	v_mfma_f32_16x16x32_bf16 v[106:109], v[186:189], v[196:199], v[106:109]
	v_mfma_f32_16x16x32_bf16 v[102:105], v[178:181], v[204:207], v[102:105]
	v_mfma_f32_16x16x32_bf16 v[98:101], v[186:189], v[204:207], v[98:101]
	v_mfma_f32_16x16x32_bf16 v[86:89], v[178:181], v[212:215], v[86:89]
	v_mfma_f32_16x16x32_bf16 v[82:85], v[186:189], v[212:215], v[82:85]
	v_mfma_f32_16x16x32_bf16 v[70:73], v[178:181], v[220:223], v[70:73]
	v_mfma_f32_16x16x32_bf16 v[66:69], v[186:189], v[220:223], v[66:69]
	v_mfma_f32_16x16x32_bf16 v[110:113], v[182:185], v[200:203], v[110:113]
	v_mfma_f32_16x16x32_bf16 v[106:109], v[192:195], v[200:203], v[106:109]
	v_mfma_f32_16x16x32_bf16 v[102:105], v[182:185], v[208:211], v[102:105]
	v_mfma_f32_16x16x32_bf16 v[98:101], v[192:195], v[208:211], v[98:101]
	v_mfma_f32_16x16x32_bf16 v[86:89], v[182:185], v[216:219], v[86:89]
	v_mfma_f32_16x16x32_bf16 v[82:85], v[192:195], v[216:219], v[82:85]
	v_mfma_f32_16x16x32_bf16 v[70:73], v[182:185], v[224:227], v[70:73]
	v_mfma_f32_16x16x32_bf16 v[66:69], v[192:195], v[224:227], v[66:69]
	s_setprio 0
	s_waitcnt vmcnt(8)
	s_barrier
	s_add_i32 s70, s60, s35
	v_lshl_add_u64 v[230:231], s[6:7], 0, v[132:133]
	s_mov_b32 m0, s70
	ds_read_b128 v[196:199], v155 offset:16384
	ds_read_b128 v[200:203], v155 offset:17408
	ds_read_b128 v[204:207], v155 offset:18432
	ds_read_b128 v[208:211], v155 offset:19456
	ds_read_b128 v[212:215], v155 offset:20480
	ds_read_b128 v[216:219], v155 offset:21504
	ds_read_b128 v[220:223], v155 offset:22528
	ds_read_b128 v[224:227], v155 offset:23552
	global_load_lds_dwordx4 v[230:231], off
	s_add_i32 m0, s70, 0x2000
	s_add_u32 s70, s6, 0x80000
	v_lshl_add_u64 v[232:233], s[6:7], 0, v[134:135]
	s_addc_u32 s71, s7, 0
	s_add_i32 s72, s61, s35
	global_load_lds_dwordx4 v[232:233], off
	v_lshl_add_u64 v[234:235], s[70:71], 0, v[132:133]
	s_mov_b32 m0, s72
	v_mov_b32_e32 v229, v137
	global_load_lds_dwordx4 v[234:235], off
	v_lshl_add_u64 v[234:235], s[70:71], 0, v[134:135]
	s_add_i32 m0, s72, 0x2000
	s_nop 0
	global_load_lds_dwordx4 v[234:235], off
	s_mov_b32 m0, s53
	v_lshl_add_u64 v[234:235], s[50:51], 0, v[136:137]
	global_load_lds_dwordx4 v136, s[50:51]
	s_mov_b32 m0, s54
	s_nop 0
	global_load_lds_dwordx4 v228, s[50:51]
	s_bitcmp1_b32 s44, 0
	s_cbranch_scc1 .Lg0skip_10
	s_waitcnt vmcnt(8)
; #define PG8_STAGE(bufoff, gbase, voff) do { _Pragma("unroll") for (int _i = 0; _i < 2; ++_i) \
;         __builtin_amdgcn_global_load_lds((const unsigned*)((const char*)(gbase) + (voff)[_i]), (LAS unsigned*)(lds + (bufoff) + ldsw + _i * 8192), 16, 0, 0); } while (0)
; #define PG8_LDA(dst, b, h) do { if constexpr (FP8) { _Pragma("unroll") for (int m = 0; m < 4; ++m) dst##8[m] = PG8_LD8(lds + PG8_SA(b, h) + aoff + m * 2048); } \
;         else { _Pragma("unroll") for (int m = 0; m < 4; ++m) _Pragma("unroll") for (int k = 0; k < 2; ++k) dst[m][k] = *(const LAS bf16x8*)(lds + PG8_SA(b, h) + aoff + m * 2048 + k * 1024); } } while (0)
; #define PG8_LDB(dst, b, h) do { if constexpr (FP8) { _Pragma("unroll") for (int n = 0; n < 2; ++n) dst##8[n] = PG8_LD8(lds + PG8_SB(b, h) + boff + n * 2048); } \
;         else { _Pragma("unroll") for (int n = 0; n < 2; ++n) _Pragma("unroll") for (int k = 0; k < 2; ++k) dst[n][k] = *(const LAS bf16x8*)(lds + PG8_SB(b, h) + boff + n * 2048 + k * 1024); } } while (0)
; #define PG8_WAIT_V(n) asm volatile("s_waitcnt vmcnt(" #n ")" ::: "memory")
; #define PG8_WAIT_L(n) asm volatile("s_waitcnt lgkmcnt(" #n ")" ::: "memory")
; #define PG8_BAR __builtin_amdgcn_s_barrier()
; #define PG8_SCHED __builtin_amdgcn_sched_barrier(0)
; template <class Epi, class Sched, bool ALIGN_EPI, bool SP2, bool FP8 = false>
; __device__ __forceinline__ void gemm_phase(LAS unsigned char* lds, const int K, const Sched& S, const Epi& E) {
;     ...
;             PG8_WAIT_V(8); PG8_WAIT_L(0); PG8_BAR; PG8_MMA(1, 0, At, B0); PG8_MMA(1, 1, At, B1); PG8_BAR; PG8_SCHED;
;             PG8_LDB(B0, 1, 0); PG8_LDB(B1, 1, 1); PG8_SCHED; PG8_LDA(At, 1, 0); PG8_STAGE(PG8_SA(0, 1), a2, vX1);
.Lg0skip_10:
	s_waitcnt lgkmcnt(0)
	v_lshl_add_u64 v[228:229], s[50:51], 0, v[228:229]
	s_setprio 1
	s_barrier
	v_mfma_f32_16x16x32_bf16 v[62:65], v[162:165], v[196:199], v[62:65]
	v_mfma_f32_16x16x32_bf16 v[58:61], v[170:173], v[196:199], v[58:61]
	v_mfma_f32_16x16x32_bf16 v[46:49], v[162:165], v[204:207], v[46:49]
	v_mfma_f32_16x16x32_bf16 v[42:45], v[170:173], v[204:207], v[42:45]
	v_mfma_f32_16x16x32_bf16 v[22:25], v[162:165], v[212:215], v[22:25]
	v_mfma_f32_16x16x32_bf16 v[18:21], v[170:173], v[212:215], v[18:21]
	v_mfma_f32_16x16x32_bf16 v[6:9], v[162:165], v[220:223], v[6:9]
	v_mfma_f32_16x16x32_bf16 v[2:5], v[170:173], v[220:223], v[2:5]
	v_mfma_f32_16x16x32_bf16 v[62:65], v[166:169], v[200:203], v[62:65]
	v_mfma_f32_16x16x32_bf16 v[58:61], v[174:177], v[200:203], v[58:61]
	v_mfma_f32_16x16x32_bf16 v[46:49], v[166:169], v[208:211], v[46:49]
	v_mfma_f32_16x16x32_bf16 v[42:45], v[174:177], v[208:211], v[42:45]
	v_mfma_f32_16x16x32_bf16 v[22:25], v[166:169], v[216:219], v[22:25]
	v_mfma_f32_16x16x32_bf16 v[18:21], v[174:177], v[216:219], v[18:21]
	v_mfma_f32_16x16x32_bf16 v[6:9], v[166:169], v[224:227], v[6:9]
	v_mfma_f32_16x16x32_bf16 v[2:5], v[174:177], v[224:227], v[2:5]
	v_mfma_f32_16x16x32_bf16 v[54:57], v[178:181], v[196:199], v[54:57]
	v_mfma_f32_16x16x32_bf16 v[50:53], v[186:189], v[196:199], v[50:53]
	v_mfma_f32_16x16x32_bf16 v[30:33], v[178:181], v[204:207], v[30:33]
	v_mfma_f32_16x16x32_bf16 v[26:29], v[186:189], v[204:207], v[26:29]
	v_mfma_f32_16x16x32_bf16 v[34:37], v[178:181], v[212:215], v[34:37]
	v_mfma_f32_16x16x32_bf16 v[38:41], v[186:189], v[212:215], v[38:41]
	v_mfma_f32_16x16x32_bf16 v[10:13], v[178:181], v[220:223], v[10:13]
	v_mfma_f32_16x16x32_bf16 v[14:17], v[186:189], v[220:223], v[14:17]
	v_mfma_f32_16x16x32_bf16 v[54:57], v[182:185], v[200:203], v[54:57]
	v_mfma_f32_16x16x32_bf16 v[50:53], v[192:195], v[200:203], v[50:53]
	v_mfma_f32_16x16x32_bf16 v[30:33], v[182:185], v[208:211], v[30:33]
	v_mfma_f32_16x16x32_bf16 v[26:29], v[192:195], v[208:211], v[26:29]
	v_mfma_f32_16x16x32_bf16 v[34:37], v[182:185], v[216:219], v[34:37]
	v_mfma_f32_16x16x32_bf16 v[38:41], v[192:195], v[216:219], v[38:41]
	v_mfma_f32_16x16x32_bf16 v[10:13], v[182:185], v[224:227], v[10:13]
	v_mfma_f32_16x16x32_bf16 v[14:17], v[192:195], v[224:227], v[14:17]
	s_setprio 0
	s_waitcnt vmcnt(8)
	s_barrier
	s_add_i32 s70, 0, 0x18000
	v_add_u32_e32 v136, s70, v151
	s_add_i32 s71, 0, 0x1c000
	ds_read_b128 v[162:165], v136
	ds_read_b128 v[166:169], v136 offset:1024
	ds_read_b128 v[170:173], v136 offset:2048
	ds_read_b128 v[174:177], v136 offset:3072
	v_add_u32_e32 v136, s71, v151
	ds_read_b128 v[178:181], v136
	ds_read_b128 v[182:185], v136 offset:1024
	ds_read_b128 v[186:189], v136 offset:2048
	ds_read_b128 v[192:195], v136 offset:3072
	s_mov_b32 m0, s55
	ds_read_b128 v[196:199], v155 offset:32768
	ds_read_b128 v[200:203], v155 offset:33792
	ds_read_b128 v[204:207], v155 offset:34816
	ds_read_b128 v[208:211], v155 offset:35840
	ds_read_b128 v[212:215], v155 offset:36864
	ds_read_b128 v[216:219], v155 offset:37888
	ds_read_b128 v[220:223], v155 offset:38912
	ds_read_b128 v[224:227], v155 offset:39936
	global_load_lds_dwordx4 v139, s[50:51]
	s_mov_b32 m0, s56
	s_nop 0
	global_load_lds_dwordx4 v141, s[50:51]
	s_bitcmp1_b32 s44, 0
	s_cbranch_scc1 .Lg0skip_11
	s_waitcnt vmcnt(8)
; #define PG8_STAGE(bufoff, gbase, voff) do { _Pragma("unroll") for (int _i = 0; _i < 2; ++_i) \
;         __builtin_amdgcn_global_load_lds((const unsigned*)((const char*)(gbase) + (voff)[_i]), (LAS unsigned*)(lds + (bufoff) + ldsw + _i * 8192), 16, 0, 0); } while (0)
; #define PG8_LDA(dst, b, h) do { if constexpr (FP8) { _Pragma("unroll") for (int m = 0; m < 4; ++m) dst##8[m] = PG8_LD8(lds + PG8_SA(b, h) + aoff + m * 2048); } \
;         else { _Pragma("unroll") for (int m = 0; m < 4; ++m) _Pragma("unroll") for (int k = 0; k < 2; ++k) dst[m][k] = *(const LAS bf16x8*)(lds + PG8_SA(b, h) + aoff + m * 2048 + k * 1024); } } while (0)
; #define PG8_WAIT_V(n) asm volatile("s_waitcnt vmcnt(" #n ")" ::: "memory")
; #define PG8_WAIT_L(n) asm volatile("s_waitcnt lgkmcnt(" #n ")" ::: "memory")
; #define PG8_BAR __builtin_amdgcn_s_barrier()
; #define PG8_SCHED __builtin_amdgcn_sched_barrier(0)
; template <class Epi, class Sched, bool ALIGN_EPI, bool SP2, bool FP8 = false>
; __device__ __forceinline__ void gemm_phase(LAS unsigned char* lds, const int K, const Sched& S, const Epi& E) {
;     ...
;             PG8_WAIT_V(8); PG8_WAIT_L(0); PG8_BAR; PG8_MMA(0, 0, At, B0); PG8_MMA(0, 1, At, B1); PG8_BAR; PG8_SCHED;
;             PG8_LDA(At, 1, 1); PG8_STAGE(PG8_SB(1, 0), b3, voffB); PG8_STAGE(PG8_SB(1, 1), b3 + hstep, voffB); PG8_STAGE(PG8_SA(1, 0), a3, vX0);
;             PG8_WAIT_V(8); PG8_WAIT_L(0); PG8_BAR; PG8_MMA(1, 0, At, B0); PG8_MMA(1, 1, At, B1); PG8_BAR; PG8_SCHED;
;         }
;         if constexpr (ALIGN_EPI) { if (wr == 0) PG8_BAR; }
.Lg0skip_11:
	s_waitcnt lgkmcnt(0)
	s_setprio 1
	s_barrier
	v_mfma_f32_16x16x32_bf16 v[126:129], v[162:165], v[196:199], v[126:129]
	v_mfma_f32_16x16x32_bf16 v[122:125], v[170:173], v[196:199], v[122:125]
	v_mfma_f32_16x16x32_bf16 v[118:121], v[162:165], v[204:207], v[118:121]
	v_mfma_f32_16x16x32_bf16 v[114:117], v[170:173], v[204:207], v[114:117]
	v_mfma_f32_16x16x32_bf16 v[94:97], v[162:165], v[212:215], v[94:97]
	v_mfma_f32_16x16x32_bf16 v[90:93], v[170:173], v[212:215], v[90:93]
	v_mfma_f32_16x16x32_bf16 v[78:81], v[162:165], v[220:223], v[78:81]
	v_mfma_f32_16x16x32_bf16 v[74:77], v[170:173], v[220:223], v[74:77]
	v_mfma_f32_16x16x32_bf16 v[126:129], v[166:169], v[200:203], v[126:129]
	v_mfma_f32_16x16x32_bf16 v[122:125], v[174:177], v[200:203], v[122:125]
	v_mfma_f32_16x16x32_bf16 v[118:121], v[166:169], v[208:211], v[118:121]
	v_mfma_f32_16x16x32_bf16 v[114:117], v[174:177], v[208:211], v[114:117]
	v_mfma_f32_16x16x32_bf16 v[94:97], v[166:169], v[216:219], v[94:97]
	v_mfma_f32_16x16x32_bf16 v[90:93], v[174:177], v[216:219], v[90:93]
	v_mfma_f32_16x16x32_bf16 v[78:81], v[166:169], v[224:227], v[78:81]
	v_mfma_f32_16x16x32_bf16 v[74:77], v[174:177], v[224:227], v[74:77]
	v_mfma_f32_16x16x32_bf16 v[110:113], v[178:181], v[196:199], v[110:113]
	v_mfma_f32_16x16x32_bf16 v[106:109], v[186:189], v[196:199], v[106:109]
	v_mfma_f32_16x16x32_bf16 v[102:105], v[178:181], v[204:207], v[102:105]
	v_mfma_f32_16x16x32_bf16 v[98:101], v[186:189], v[204:207], v[98:101]
	v_mfma_f32_16x16x32_bf16 v[86:89], v[178:181], v[212:215], v[86:89]
	v_mfma_f32_16x16x32_bf16 v[82:85], v[186:189], v[212:215], v[82:85]
	v_mfma_f32_16x16x32_bf16 v[70:73], v[178:181], v[220:223], v[70:73]
	v_mfma_f32_16x16x32_bf16 v[66:69], v[186:189], v[220:223], v[66:69]
	v_mfma_f32_16x16x32_bf16 v[110:113], v[182:185], v[200:203], v[110:113]
	v_mfma_f32_16x16x32_bf16 v[106:109], v[192:195], v[200:203], v[106:109]
	v_mfma_f32_16x16x32_bf16 v[102:105], v[182:185], v[208:211], v[102:105]
	v_mfma_f32_16x16x32_bf16 v[98:101], v[192:195], v[208:211], v[98:101]
	v_mfma_f32_16x16x32_bf16 v[86:89], v[182:185], v[216:219], v[86:89]
	v_mfma_f32_16x16x32_bf16 v[82:85], v[192:195], v[216:219], v[82:85]
	v_mfma_f32_16x16x32_bf16 v[70:73], v[182:185], v[224:227], v[70:73]
	v_mfma_f32_16x16x32_bf16 v[66:69], v[192:195], v[224:227], v[66:69]
	s_setprio 0
	s_waitcnt vmcnt(8)
	s_barrier
	s_add_i32 s50, s70, s35
	v_lshl_add_u64 v[230:231], v[230:231], 0, s[40:41]
	s_mov_b32 m0, s50
	ds_read_b128 v[196:199], v155 offset:49152
	ds_read_b128 v[200:203], v155 offset:50176
	ds_read_b128 v[204:207], v155 offset:51200
	ds_read_b128 v[208:211], v155 offset:52224
	ds_read_b128 v[212:215], v155 offset:53248
	ds_read_b128 v[216:219], v155 offset:54272
	ds_read_b128 v[220:223], v155 offset:55296
	ds_read_b128 v[224:227], v155 offset:56320
	global_load_lds_dwordx4 v[230:231], off
	s_add_i32 m0, s50, 0x2000
	s_add_u32 s6, s6, 0x80080
	v_lshl_add_u64 v[230:231], v[232:233], 0, s[40:41]
	s_addc_u32 s7, s7, 0
	s_add_i32 s50, s71, s35
	global_load_lds_dwordx4 v[230:231], off
	v_lshl_add_u64 v[230:231], s[6:7], 0, v[132:133]
	s_mov_b32 m0, s50
	v_lshl_add_u64 v[228:229], v[228:229], 0, s[40:41]
	global_load_lds_dwordx4 v[230:231], off
	v_lshl_add_u64 v[230:231], s[6:7], 0, v[134:135]
	s_add_i32 m0, s50, 0x2000
	s_nop 0
	global_load_lds_dwordx4 v[230:231], off
	v_lshl_add_u64 v[230:231], v[234:235], 0, s[40:41]
	s_mov_b32 m0, s58
	s_nop 0
	global_load_lds_dwordx4 v[230:231], off
	s_mov_b32 m0, s59
	s_nop 0
	global_load_lds_dwordx4 v[228:229], off
	s_bitcmp1_b32 s44, 0
	s_cbranch_scc1 .Lg0skip_12
	s_waitcnt vmcnt(8)
.Lg0skip_12:
	s_waitcnt lgkmcnt(0)
	s_setprio 1
	s_barrier
	v_mfma_f32_16x16x32_bf16 v[62:65], v[162:165], v[196:199], v[62:65]
	v_mfma_f32_16x16x32_bf16 v[58:61], v[170:173], v[196:199], v[58:61]
	v_mfma_f32_16x16x32_bf16 v[46:49], v[162:165], v[204:207], v[46:49]
	v_mfma_f32_16x16x32_bf16 v[42:45], v[170:173], v[204:207], v[42:45]
	v_mfma_f32_16x16x32_bf16 v[22:25], v[162:165], v[212:215], v[22:25]
	v_mfma_f32_16x16x32_bf16 v[18:21], v[170:173], v[212:215], v[18:21]
	v_mfma_f32_16x16x32_bf16 v[6:9], v[162:165], v[220:223], v[6:9]
	v_mfma_f32_16x16x32_bf16 v[2:5], v[170:173], v[220:223], v[2:5]
	v_mfma_f32_16x16x32_bf16 v[62:65], v[166:169], v[200:203], v[62:65]
	v_mfma_f32_16x16x32_bf16 v[58:61], v[174:177], v[200:203], v[58:61]
	v_mfma_f32_16x16x32_bf16 v[46:49], v[166:169], v[208:211], v[46:49]
	v_mfma_f32_16x16x32_bf16 v[42:45], v[174:177], v[208:211], v[42:45]
	v_mfma_f32_16x16x32_bf16 v[22:25], v[166:169], v[216:219], v[22:25]
	v_mfma_f32_16x16x32_bf16 v[18:21], v[174:177], v[216:219], v[18:21]
	v_mfma_f32_16x16x32_bf16 v[6:9], v[166:169], v[224:227], v[6:9]
	v_mfma_f32_16x16x32_bf16 v[2:5], v[174:177], v[224:227], v[2:5]
	v_mfma_f32_16x16x32_bf16 v[54:57], v[178:181], v[196:199], v[54:57]
	v_mfma_f32_16x16x32_bf16 v[50:53], v[186:189], v[196:199], v[50:53]
	v_mfma_f32_16x16x32_bf16 v[30:33], v[178:181], v[204:207], v[30:33]
	v_mfma_f32_16x16x32_bf16 v[26:29], v[186:189], v[204:207], v[26:29]
	v_mfma_f32_16x16x32_bf16 v[34:37], v[178:181], v[212:215], v[34:37]
	v_mfma_f32_16x16x32_bf16 v[38:41], v[186:189], v[212:215], v[38:41]
	v_mfma_f32_16x16x32_bf16 v[10:13], v[178:181], v[220:223], v[10:13]
	v_mfma_f32_16x16x32_bf16 v[14:17], v[186:189], v[220:223], v[14:17]
	v_mfma_f32_16x16x32_bf16 v[54:57], v[182:185], v[200:203], v[54:57]
	v_mfma_f32_16x16x32_bf16 v[50:53], v[192:195], v[200:203], v[50:53]
	v_mfma_f32_16x16x32_bf16 v[30:33], v[182:185], v[208:211], v[30:33]
	v_mfma_f32_16x16x32_bf16 v[26:29], v[192:195], v[208:211], v[26:29]
	v_mfma_f32_16x16x32_bf16 v[34:37], v[182:185], v[216:219], v[34:37]
	v_mfma_f32_16x16x32_bf16 v[38:41], v[192:195], v[216:219], v[38:41]
	v_mfma_f32_16x16x32_bf16 v[10:13], v[182:185], v[224:227], v[10:13]
	v_mfma_f32_16x16x32_bf16 v[14:17], v[192:195], v[224:227], v[14:17]
	s_setprio 0
	s_waitcnt vmcnt(8)
	s_barrier
	s_add_i32 s69, s69, 2
	s_add_u32 s4, s4, 0x100
	s_addc_u32 s5, s5, 0
	s_cmp_gt_u32 s69, 29
	s_cbranch_scc0 .LBB0_883
	s_and_b64 vcc, exec, s[44:45]
	s_cbranch_vccz .LBB0_886
	s_barrier

; #define PG8_STAGE(bufoff, gbase, voff) do { _Pragma("unroll") for (int _i = 0; _i < 2; ++_i) \
;         __builtin_amdgcn_global_load_lds((const unsigned*)((const char*)(gbase) + (voff)[_i]), (LAS unsigned*)(lds + (bufoff) + ldsw + _i * 8192), 16, 0, 0); } while (0)
; #define PG8_LDA(dst, b, h) do { if constexpr (FP8) { _Pragma("unroll") for (int m = 0; m < 4; ++m) dst##8[m] = PG8_LD8(lds + PG8_SA(b, h) + aoff + m * 2048); } \
;         else { _Pragma("unroll") for (int m = 0; m < 4; ++m) _Pragma("unroll") for (int k = 0; k < 2; ++k) dst[m][k] = *(const LAS bf16x8*)(lds + PG8_SA(b, h) + aoff + m * 2048 + k * 1024); } } while (0)
; #define PG8_LDB(dst, b, h) do { if constexpr (FP8) { _Pragma("unroll") for (int n = 0; n < 2; ++n) dst##8[n] = PG8_LD8(lds + PG8_SB(b, h) + boff + n * 2048); } \
;         else { _Pragma("unroll") for (int n = 0; n < 2; ++n) _Pragma("unroll") for (int k = 0; k < 2; ++k) dst[n][k] = *(const LAS bf16x8*)(lds + PG8_SB(b, h) + boff + n * 2048 + k * 1024); } } while (0)
; #define PG8_WAIT_V(n) asm volatile("s_waitcnt vmcnt(" #n ")" ::: "memory")
; #define PG8_WAIT_L(n) asm volatile("s_waitcnt lgkmcnt(" #n ")" ::: "memory")
; #define PG8_BAR __builtin_amdgcn_s_barrier()
; #define PG8_SCHED __builtin_amdgcn_sched_barrier(0)
; template <class Epi, class Sched, bool ALIGN_EPI, bool SP2, bool FP8 = false>
; __device__ __forceinline__ void gemm_phase(LAS unsigned char* lds, const int K, const Sched& S, const Epi& E) {
;     ...
;         for (int t = 0; t < nt; t += 2) {
;             const bool last = (t == nt - 2);
;             const char* a1 = cA + (size_t)(t + 1) * kstep;
;             const char* a2 = last ? nA : cA + (size_t)(t + 2) * kstep; const char* b2 = last ? nB : cB + (size_t)(t + 2) * kstep;
;             const char* a3 = a2 + kstep; const char* b3 = b2 + kstep;
;             unsigned vX0[2], vX1[2];
; #pragma unroll
;             for (int i = 0; i < 2; ++i) { vX0[i] = last ? vAn[0][i] : vAc[0][i]; vX1[i] = last ? vAn[1][i] : vAc[1][i]; }
;             PG8_LDB(B0, 0, 0); PG8_LDB(B1, 0, 1); PG8_SCHED; PG8_LDA(At, 0, 0); PG8_STAGE(PG8_SA(1, 1), a1, vAc[1]);
;             PG8_WAIT_V(8); PG8_WAIT_L(0); PG8_BAR; PG8_MMA(0, 0, At, B0); PG8_MMA(0, 1, At, B1); PG8_BAR; PG8_SCHED;
;             PG8_LDA(At, 0, 1); PG8_STAGE(PG8_SB(0, 0), b2, voffB); PG8_STAGE(PG8_SB(0, 1), b2 + hstep, voffB); PG8_STAGE(PG8_SA(0, 0), a2, vX0);
.LBB0_1025:
	ds_read_b128 v[140:143], v182
	ds_read_b128 v[144:147], v182 offset:1024
	ds_read_b128 v[148:151], v182 offset:2048
	ds_read_b128 v[160:163], v182 offset:3072
	ds_read_b128 v[164:167], v183
	ds_read_b128 v[168:171], v183 offset:1024
	ds_read_b128 v[172:175], v183 offset:2048
	ds_read_b128 v[192:195], v183 offset:3072
	s_add_u32 s56, s30, s50
	s_addc_u32 s57, s31, s51
	s_add_u32 s58, s56, 0x23000100
	s_addc_u32 s59, s57, 0
	s_add_u32 s69, s45, s50
	s_addc_u32 s70, s49, s51
	s_cmpk_eq_i32 s50, 0x300
	s_cselect_b64 vcc, -1, 0
	s_and_b64 s[56:57], vcc, exec
	v_cndmask_b32_e32 v158, v135, v186, vcc
	s_cselect_b32 s59, s9, s59
	s_cselect_b32 s58, s8, s58
	v_cndmask_b32_e32 v131, v130, v187, vcc
	v_cndmask_b32_e32 v152, v134, v188, vcc
	v_cndmask_b32_e32 v133, v132, v189, vcc
	s_cselect_b32 s57, s47, s70
	s_cselect_b32 s56, s46, s69
	v_lshl_add_u64 v[176:177], v[138:139], 0, s[50:51]
	s_add_i32 m0, s53, 0xc000
	ds_read_b128 v[196:199], v184
	ds_read_b128 v[200:203], v184 offset:1024
	ds_read_b128 v[204:207], v184 offset:2048
	ds_read_b128 v[208:211], v184 offset:3072
	ds_read_b128 v[212:215], v184 offset:4096
	ds_read_b128 v[216:219], v184 offset:5120
	ds_read_b128 v[220:223], v184 offset:6144
	ds_read_b128 v[224:227], v184 offset:7168
	global_load_lds_dwordx4 v[176:177], off
	v_lshl_add_u64 v[176:177], v[136:137], 0, s[50:51]
	s_add_i32 m0, s53, 0xe000
	s_nop 0
	global_load_lds_dwordx4 v[176:177], off
	s_bitcmp1_b32 s42, 0
	s_cbranch_scc1 .Lg0skip_13
	s_waitcnt vmcnt(8)
.Lg0skip_13:
	s_waitcnt lgkmcnt(0)
	s_setprio 1
	s_barrier
	v_mfma_f32_16x16x32_bf16 v[126:129], v[140:143], v[196:199], v[126:129]
	v_mfma_f32_16x16x32_bf16 v[122:125], v[148:151], v[196:199], v[122:125]
	v_mfma_f32_16x16x32_bf16 v[110:113], v[140:143], v[204:207], v[110:113]
	v_mfma_f32_16x16x32_bf16 v[106:109], v[148:151], v[204:207], v[106:109]
	v_mfma_f32_16x16x32_bf16 v[94:97], v[140:143], v[212:215], v[94:97]
	v_mfma_f32_16x16x32_bf16 v[90:93], v[148:151], v[212:215], v[90:93]
	v_mfma_f32_16x16x32_bf16 v[78:81], v[140:143], v[220:223], v[78:81]
	v_mfma_f32_16x16x32_bf16 v[74:77], v[148:151], v[220:223], v[74:77]
	v_mfma_f32_16x16x32_bf16 v[126:129], v[144:147], v[200:203], v[126:129]
	v_mfma_f32_16x16x32_bf16 v[122:125], v[160:163], v[200:203], v[122:125]
	v_mfma_f32_16x16x32_bf16 v[110:113], v[144:147], v[208:211], v[110:113]
	v_mfma_f32_16x16x32_bf16 v[106:109], v[160:163], v[208:211], v[106:109]
	v_mfma_f32_16x16x32_bf16 v[94:97], v[144:147], v[216:219], v[94:97]
	v_mfma_f32_16x16x32_bf16 v[90:93], v[160:163], v[216:219], v[90:93]
	v_mfma_f32_16x16x32_bf16 v[78:81], v[144:147], v[224:227], v[78:81]
	v_mfma_f32_16x16x32_bf16 v[74:77], v[160:163], v[224:227], v[74:77]
	v_mfma_f32_16x16x32_bf16 v[118:121], v[164:167], v[196:199], v[118:121]
	v_mfma_f32_16x16x32_bf16 v[114:117], v[172:175], v[196:199], v[114:117]
	v_mfma_f32_16x16x32_bf16 v[102:105], v[164:167], v[204:207], v[102:105]
	v_mfma_f32_16x16x32_bf16 v[98:101], v[172:175], v[204:207], v[98:101]
	v_mfma_f32_16x16x32_bf16 v[86:89], v[164:167], v[212:215], v[86:89]
	v_mfma_f32_16x16x32_bf16 v[82:85], v[172:175], v[212:215], v[82:85]
	v_mfma_f32_16x16x32_bf16 v[70:73], v[164:167], v[220:223], v[70:73]
	v_mfma_f32_16x16x32_bf16 v[66:69], v[172:175], v[220:223], v[66:69]
	v_mfma_f32_16x16x32_bf16 v[118:121], v[168:171], v[200:203], v[118:121]
	v_mfma_f32_16x16x32_bf16 v[114:117], v[192:195], v[200:203], v[114:117]
	v_mfma_f32_16x16x32_bf16 v[102:105], v[168:171], v[208:211], v[102:105]
	v_mfma_f32_16x16x32_bf16 v[98:101], v[192:195], v[208:211], v[98:101]
	v_mfma_f32_16x16x32_bf16 v[86:89], v[168:171], v[216:219], v[86:89]
	v_mfma_f32_16x16x32_bf16 v[82:85], v[192:195], v[216:219], v[82:85]
	v_mfma_f32_16x16x32_bf16 v[70:73], v[168:171], v[224:227], v[70:73]
	v_mfma_f32_16x16x32_bf16 v[66:69], v[192:195], v[224:227], v[66:69]
	s_setprio 0
	s_waitcnt vmcnt(8)
	s_barrier
	s_add_i32 s69, s64, s35
	v_lshl_add_u64 v[176:177], s[56:57], 0, v[154:155]
	s_mov_b32 m0, s69
	ds_read_b128 v[196:199], v184 offset:16384
	ds_read_b128 v[200:203], v184 offset:17408
	ds_read_b128 v[204:207], v184 offset:18432
	ds_read_b128 v[208:211], v184 offset:19456
	ds_read_b128 v[212:215], v184 offset:20480
	ds_read_b128 v[216:219], v184 offset:21504
	ds_read_b128 v[220:223], v184 offset:22528
	ds_read_b128 v[224:227], v184 offset:23552
	global_load_lds_dwordx4 v[176:177], off
	s_add_i32 m0, s69, 0x2000
	s_add_u32 s70, s56, 0x20000
	v_lshl_add_u64 v[228:229], s[56:57], 0, v[156:157]
	s_addc_u32 s71, s57, 0
	s_add_i32 s69, s65, s35
	global_load_lds_dwordx4 v[228:229], off
	v_lshl_add_u64 v[230:231], s[70:71], 0, v[154:155]
	s_mov_b32 m0, s69
	v_mov_b32_e32 v153, v159
	global_load_lds_dwordx4 v[230:231], off
	v_lshl_add_u64 v[230:231], s[70:71], 0, v[156:157]
	s_add_i32 m0, s69, 0x2000
	s_nop 0
	global_load_lds_dwordx4 v[230:231], off
	s_mov_b32 m0, s53
	v_lshl_add_u64 v[230:231], s[58:59], 0, v[158:159]
	global_load_lds_dwordx4 v158, s[58:59]
	s_mov_b32 m0, s54
	s_nop 0
	global_load_lds_dwordx4 v152, s[58:59]
	s_bitcmp1_b32 s42, 0
	s_cbranch_scc1 .Lg0skip_14
	s_waitcnt vmcnt(8)
; #define PG8_STAGE(bufoff, gbase, voff) do { _Pragma("unroll") for (int _i = 0; _i < 2; ++_i) \
;         __builtin_amdgcn_global_load_lds((const unsigned*)((const char*)(gbase) + (voff)[_i]), (LAS unsigned*)(lds + (bufoff) + ldsw + _i * 8192), 16, 0, 0); } while (0)
; #define PG8_LDA(dst, b, h) do { if constexpr (FP8) { _Pragma("unroll") for (int m = 0; m < 4; ++m) dst##8[m] = PG8_LD8(lds + PG8_SA(b, h) + aoff + m * 2048); } \
;         else { _Pragma("unroll") for (int m = 0; m < 4; ++m) _Pragma("unroll") for (int k = 0; k < 2; ++k) dst[m][k] = *(const LAS bf16x8*)(lds + PG8_SA(b, h) + aoff + m * 2048 + k * 1024); } } while (0)
; #define PG8_LDB(dst, b, h) do { if constexpr (FP8) { _Pragma("unroll") for (int n = 0; n < 2; ++n) dst##8[n] = PG8_LD8(lds + PG8_SB(b, h) + boff + n * 2048); } \
;         else { _Pragma("unroll") for (int n = 0; n < 2; ++n) _Pragma("unroll") for (int k = 0; k < 2; ++k) dst[n][k] = *(const LAS bf16x8*)(lds + PG8_SB(b, h) + boff + n * 2048 + k * 1024); } } while (0)
; #define PG8_WAIT_V(n) asm volatile("s_waitcnt vmcnt(" #n ")" ::: "memory")
; #define PG8_WAIT_L(n) asm volatile("s_waitcnt lgkmcnt(" #n ")" ::: "memory")
; #define PG8_BAR __builtin_amdgcn_s_barrier()
; #define PG8_SCHED __builtin_amdgcn_sched_barrier(0)
; template <class Epi, class Sched, bool ALIGN_EPI, bool SP2, bool FP8 = false>
; __device__ __forceinline__ void gemm_phase(LAS unsigned char* lds, const int K, const Sched& S, const Epi& E) {
;     ...
;             PG8_WAIT_V(8); PG8_WAIT_L(0); PG8_BAR; PG8_MMA(1, 0, At, B0); PG8_MMA(1, 1, At, B1); PG8_BAR; PG8_SCHED;
;             PG8_LDB(B0, 1, 0); PG8_LDB(B1, 1, 1); PG8_SCHED; PG8_LDA(At, 1, 0); PG8_STAGE(PG8_SA(0, 1), a2, vX1);
.Lg0skip_14:
	s_waitcnt lgkmcnt(0)
	v_lshl_add_u64 v[152:153], s[58:59], 0, v[152:153]
	s_setprio 1
	s_barrier
	v_mfma_f32_16x16x32_bf16 v[62:65], v[140:143], v[196:199], v[62:65]
	v_mfma_f32_16x16x32_bf16 v[58:61], v[148:151], v[196:199], v[58:61]
	v_mfma_f32_16x16x32_bf16 v[46:49], v[140:143], v[204:207], v[46:49]
	v_mfma_f32_16x16x32_bf16 v[42:45], v[148:151], v[204:207], v[42:45]
	v_mfma_f32_16x16x32_bf16 v[22:25], v[140:143], v[212:215], v[22:25]
	v_mfma_f32_16x16x32_bf16 v[18:21], v[148:151], v[212:215], v[18:21]
	v_mfma_f32_16x16x32_bf16 v[6:9], v[140:143], v[220:223], v[6:9]
	v_mfma_f32_16x16x32_bf16 v[2:5], v[148:151], v[220:223], v[2:5]
	v_mfma_f32_16x16x32_bf16 v[62:65], v[144:147], v[200:203], v[62:65]
	v_mfma_f32_16x16x32_bf16 v[58:61], v[160:163], v[200:203], v[58:61]
	v_mfma_f32_16x16x32_bf16 v[46:49], v[144:147], v[208:211], v[46:49]
	v_mfma_f32_16x16x32_bf16 v[42:45], v[160:163], v[208:211], v[42:45]
	v_mfma_f32_16x16x32_bf16 v[22:25], v[144:147], v[216:219], v[22:25]
	v_mfma_f32_16x16x32_bf16 v[18:21], v[160:163], v[216:219], v[18:21]
	v_mfma_f32_16x16x32_bf16 v[6:9], v[144:147], v[224:227], v[6:9]
	v_mfma_f32_16x16x32_bf16 v[2:5], v[160:163], v[224:227], v[2:5]
	v_mfma_f32_16x16x32_bf16 v[54:57], v[164:167], v[196:199], v[54:57]
	v_mfma_f32_16x16x32_bf16 v[50:53], v[172:175], v[196:199], v[50:53]
	v_mfma_f32_16x16x32_bf16 v[38:41], v[164:167], v[204:207], v[38:41]
	v_mfma_f32_16x16x32_bf16 v[34:37], v[172:175], v[204:207], v[34:37]
	v_mfma_f32_16x16x32_bf16 v[30:33], v[164:167], v[212:215], v[30:33]
	v_mfma_f32_16x16x32_bf16 v[26:29], v[172:175], v[212:215], v[26:29]
	v_mfma_f32_16x16x32_bf16 v[14:17], v[164:167], v[220:223], v[14:17]
	v_mfma_f32_16x16x32_bf16 v[10:13], v[172:175], v[220:223], v[10:13]
	v_mfma_f32_16x16x32_bf16 v[54:57], v[168:171], v[200:203], v[54:57]
	v_mfma_f32_16x16x32_bf16 v[50:53], v[192:195], v[200:203], v[50:53]
	v_mfma_f32_16x16x32_bf16 v[38:41], v[168:171], v[208:211], v[38:41]
	v_mfma_f32_16x16x32_bf16 v[34:37], v[192:195], v[208:211], v[34:37]
	v_mfma_f32_16x16x32_bf16 v[30:33], v[168:171], v[216:219], v[30:33]
	v_mfma_f32_16x16x32_bf16 v[26:29], v[192:195], v[216:219], v[26:29]
	v_mfma_f32_16x16x32_bf16 v[14:17], v[168:171], v[224:227], v[14:17]
	v_mfma_f32_16x16x32_bf16 v[10:13], v[192:195], v[224:227], v[10:13]
	s_setprio 0
	s_waitcnt vmcnt(8)
	s_barrier
	s_add_i32 s69, 0, 0x18000
	v_add_u32_e32 v158, s69, v180
	s_add_i32 s70, 0, 0x1c000
	ds_read_b128 v[140:143], v158
	ds_read_b128 v[144:147], v158 offset:1024
	ds_read_b128 v[148:151], v158 offset:2048
	ds_read_b128 v[160:163], v158 offset:3072
	v_add_u32_e32 v158, s70, v180
	ds_read_b128 v[164:167], v158
	ds_read_b128 v[168:171], v158 offset:1024
	ds_read_b128 v[172:175], v158 offset:2048
	ds_read_b128 v[192:195], v158 offset:3072
	s_mov_b32 m0, s55
	ds_read_b128 v[196:199], v184 offset:32768
	ds_read_b128 v[200:203], v184 offset:33792
	ds_read_b128 v[204:207], v184 offset:34816
	ds_read_b128 v[208:211], v184 offset:35840
	ds_read_b128 v[212:215], v184 offset:36864
	ds_read_b128 v[216:219], v184 offset:37888
	ds_read_b128 v[220:223], v184 offset:38912
	ds_read_b128 v[224:227], v184 offset:39936
	global_load_lds_dwordx4 v131, s[58:59]
	s_mov_b32 m0, s60
	s_nop 0
	global_load_lds_dwordx4 v133, s[58:59]
	s_bitcmp1_b32 s42, 0
	s_cbranch_scc1 .Lg0skip_15
	s_waitcnt vmcnt(8)
; #define PG8_STAGE(bufoff, gbase, voff) do { _Pragma("unroll") for (int _i = 0; _i < 2; ++_i) \
;         __builtin_amdgcn_global_load_lds((const unsigned*)((const char*)(gbase) + (voff)[_i]), (LAS unsigned*)(lds + (bufoff) + ldsw + _i * 8192), 16, 0, 0); } while (0)
; #define PG8_LDA(dst, b, h) do { if constexpr (FP8) { _Pragma("unroll") for (int m = 0; m < 4; ++m) dst##8[m] = PG8_LD8(lds + PG8_SA(b, h) + aoff + m * 2048); } \
;         else { _Pragma("unroll") for (int m = 0; m < 4; ++m) _Pragma("unroll") for (int k = 0; k < 2; ++k) dst[m][k] = *(const LAS bf16x8*)(lds + PG8_SA(b, h) + aoff + m * 2048 + k * 1024); } } while (0)
; #define PG8_WAIT_V(n) asm volatile("s_waitcnt vmcnt(" #n ")" ::: "memory")
; #define PG8_WAIT_L(n) asm volatile("s_waitcnt lgkmcnt(" #n ")" ::: "memory")
; #define PG8_BAR __builtin_amdgcn_s_barrier()
; #define PG8_SCHED __builtin_amdgcn_sched_barrier(0)
; template <class Epi, class Sched, bool ALIGN_EPI, bool SP2, bool FP8 = false>
; __device__ __forceinline__ void gemm_phase(LAS unsigned char* lds, const int K, const Sched& S, const Epi& E) {
;     ...
;             PG8_WAIT_V(8); PG8_WAIT_L(0); PG8_BAR; PG8_MMA(0, 0, At, B0); PG8_MMA(0, 1, At, B1); PG8_BAR; PG8_SCHED;
;             PG8_LDA(At, 1, 1); PG8_STAGE(PG8_SB(1, 0), b3, voffB); PG8_STAGE(PG8_SB(1, 1), b3 + hstep, voffB); PG8_STAGE(PG8_SA(1, 0), a3, vX0);
;             PG8_WAIT_V(8); PG8_WAIT_L(0); PG8_BAR; PG8_MMA(1, 0, At, B0); PG8_MMA(1, 1, At, B1); PG8_BAR; PG8_SCHED;
;         }
;         if constexpr (ALIGN_EPI) { if (wr == 0) PG8_BAR; }
.Lg0skip_15:
	s_waitcnt lgkmcnt(0)
	s_setprio 1
	s_barrier
	v_mfma_f32_16x16x32_bf16 v[126:129], v[140:143], v[196:199], v[126:129]
	v_mfma_f32_16x16x32_bf16 v[122:125], v[148:151], v[196:199], v[122:125]
	v_mfma_f32_16x16x32_bf16 v[110:113], v[140:143], v[204:207], v[110:113]
	v_mfma_f32_16x16x32_bf16 v[106:109], v[148:151], v[204:207], v[106:109]
	v_mfma_f32_16x16x32_bf16 v[94:97], v[140:143], v[212:215], v[94:97]
	v_mfma_f32_16x16x32_bf16 v[90:93], v[148:151], v[212:215], v[90:93]
	v_mfma_f32_16x16x32_bf16 v[78:81], v[140:143], v[220:223], v[78:81]
	v_mfma_f32_16x16x32_bf16 v[74:77], v[148:151], v[220:223], v[74:77]
	v_mfma_f32_16x16x32_bf16 v[126:129], v[144:147], v[200:203], v[126:129]
	v_mfma_f32_16x16x32_bf16 v[122:125], v[160:163], v[200:203], v[122:125]
	v_mfma_f32_16x16x32_bf16 v[110:113], v[144:147], v[208:211], v[110:113]
	v_mfma_f32_16x16x32_bf16 v[106:109], v[160:163], v[208:211], v[106:109]
	v_mfma_f32_16x16x32_bf16 v[94:97], v[144:147], v[216:219], v[94:97]
	v_mfma_f32_16x16x32_bf16 v[90:93], v[160:163], v[216:219], v[90:93]
	v_mfma_f32_16x16x32_bf16 v[78:81], v[144:147], v[224:227], v[78:81]
	v_mfma_f32_16x16x32_bf16 v[74:77], v[160:163], v[224:227], v[74:77]
	v_mfma_f32_16x16x32_bf16 v[118:121], v[164:167], v[196:199], v[118:121]
	v_mfma_f32_16x16x32_bf16 v[114:117], v[172:175], v[196:199], v[114:117]
	v_mfma_f32_16x16x32_bf16 v[102:105], v[164:167], v[204:207], v[102:105]
	v_mfma_f32_16x16x32_bf16 v[98:101], v[172:175], v[204:207], v[98:101]
	v_mfma_f32_16x16x32_bf16 v[86:89], v[164:167], v[212:215], v[86:89]
	v_mfma_f32_16x16x32_bf16 v[82:85], v[172:175], v[212:215], v[82:85]
	v_mfma_f32_16x16x32_bf16 v[70:73], v[164:167], v[220:223], v[70:73]
	v_mfma_f32_16x16x32_bf16 v[66:69], v[172:175], v[220:223], v[66:69]
	v_mfma_f32_16x16x32_bf16 v[118:121], v[168:171], v[200:203], v[118:121]
	v_mfma_f32_16x16x32_bf16 v[114:117], v[192:195], v[200:203], v[114:117]
	v_mfma_f32_16x16x32_bf16 v[102:105], v[168:171], v[208:211], v[102:105]
	v_mfma_f32_16x16x32_bf16 v[98:101], v[192:195], v[208:211], v[98:101]
	v_mfma_f32_16x16x32_bf16 v[86:89], v[168:171], v[216:219], v[86:89]
	v_mfma_f32_16x16x32_bf16 v[82:85], v[192:195], v[216:219], v[82:85]
	v_mfma_f32_16x16x32_bf16 v[70:73], v[168:171], v[224:227], v[70:73]
	v_mfma_f32_16x16x32_bf16 v[66:69], v[192:195], v[224:227], v[66:69]
	s_setprio 0
	s_waitcnt vmcnt(8)
	s_barrier
	s_add_i32 s58, s69, s35
	v_lshl_add_u64 v[176:177], v[176:177], 0, s[38:39]
	s_mov_b32 m0, s58
	ds_read_b128 v[196:199], v184 offset:49152
	ds_read_b128 v[200:203], v184 offset:50176
	ds_read_b128 v[204:207], v184 offset:51200
	ds_read_b128 v[208:211], v184 offset:52224
	ds_read_b128 v[212:215], v184 offset:53248
	ds_read_b128 v[216:219], v184 offset:54272
	ds_read_b128 v[220:223], v184 offset:55296
	ds_read_b128 v[224:227], v184 offset:56320
	global_load_lds_dwordx4 v[176:177], off
	s_add_i32 m0, s58, 0x2000
	s_add_u32 s56, s56, 0x20080
	v_lshl_add_u64 v[176:177], v[228:229], 0, s[38:39]
	s_addc_u32 s57, s57, 0
	s_add_i32 s58, s70, s35
	global_load_lds_dwordx4 v[176:177], off
	v_lshl_add_u64 v[176:177], s[56:57], 0, v[154:155]
	s_mov_b32 m0, s58
	v_lshl_add_u64 v[152:153], v[152:153], 0, s[38:39]
	global_load_lds_dwordx4 v[176:177], off
	v_lshl_add_u64 v[176:177], s[56:57], 0, v[156:157]
	s_add_i32 m0, s58, 0x2000
	s_nop 0
	global_load_lds_dwordx4 v[176:177], off
	v_lshl_add_u64 v[176:177], v[230:231], 0, s[38:39]
	s_mov_b32 m0, s62
	s_nop 0
	global_load_lds_dwordx4 v[176:177], off
	s_mov_b32 m0, s63
	s_nop 0
	global_load_lds_dwordx4 v[152:153], off
	s_bitcmp1_b32 s42, 0
	s_cbranch_scc1 .Lg0skip_16
	s_waitcnt vmcnt(8)
.Lg0skip_16:
	s_waitcnt lgkmcnt(0)
	s_setprio 1
	s_barrier
	v_mfma_f32_16x16x32_bf16 v[62:65], v[140:143], v[196:199], v[62:65]
	v_mfma_f32_16x16x32_bf16 v[58:61], v[148:151], v[196:199], v[58:61]
	v_mfma_f32_16x16x32_bf16 v[46:49], v[140:143], v[204:207], v[46:49]
	v_mfma_f32_16x16x32_bf16 v[42:45], v[148:151], v[204:207], v[42:45]
	v_mfma_f32_16x16x32_bf16 v[22:25], v[140:143], v[212:215], v[22:25]
	v_mfma_f32_16x16x32_bf16 v[18:21], v[148:151], v[212:215], v[18:21]
	v_mfma_f32_16x16x32_bf16 v[6:9], v[140:143], v[220:223], v[6:9]
	v_mfma_f32_16x16x32_bf16 v[2:5], v[148:151], v[220:223], v[2:5]
	v_mfma_f32_16x16x32_bf16 v[62:65], v[144:147], v[200:203], v[62:65]
	v_mfma_f32_16x16x32_bf16 v[58:61], v[160:163], v[200:203], v[58:61]
	v_mfma_f32_16x16x32_bf16 v[46:49], v[144:147], v[208:211], v[46:49]
	v_mfma_f32_16x16x32_bf16 v[42:45], v[160:163], v[208:211], v[42:45]
	v_mfma_f32_16x16x32_bf16 v[22:25], v[144:147], v[216:219], v[22:25]
	v_mfma_f32_16x16x32_bf16 v[18:21], v[160:163], v[216:219], v[18:21]
	v_mfma_f32_16x16x32_bf16 v[6:9], v[144:147], v[224:227], v[6:9]
	v_mfma_f32_16x16x32_bf16 v[2:5], v[160:163], v[224:227], v[2:5]
	v_mfma_f32_16x16x32_bf16 v[54:57], v[164:167], v[196:199], v[54:57]
	v_mfma_f32_16x16x32_bf16 v[50:53], v[172:175], v[196:199], v[50:53]
	v_mfma_f32_16x16x32_bf16 v[38:41], v[164:167], v[204:207], v[38:41]
	v_mfma_f32_16x16x32_bf16 v[34:37], v[172:175], v[204:207], v[34:37]
	v_mfma_f32_16x16x32_bf16 v[30:33], v[164:167], v[212:215], v[30:33]
	v_mfma_f32_16x16x32_bf16 v[26:29], v[172:175], v[212:215], v[26:29]
	v_mfma_f32_16x16x32_bf16 v[14:17], v[164:167], v[220:223], v[14:17]
	v_mfma_f32_16x16x32_bf16 v[10:13], v[172:175], v[220:223], v[10:13]
	v_mfma_f32_16x16x32_bf16 v[54:57], v[168:171], v[200:203], v[54:57]
	v_mfma_f32_16x16x32_bf16 v[50:53], v[192:195], v[200:203], v[50:53]
	v_mfma_f32_16x16x32_bf16 v[38:41], v[168:171], v[208:211], v[38:41]
	v_mfma_f32_16x16x32_bf16 v[34:37], v[192:195], v[208:211], v[34:37]
	v_mfma_f32_16x16x32_bf16 v[30:33], v[168:171], v[216:219], v[30:33]
	v_mfma_f32_16x16x32_bf16 v[26:29], v[192:195], v[216:219], v[26:29]
	v_mfma_f32_16x16x32_bf16 v[14:17], v[168:171], v[224:227], v[14:17]
	v_mfma_f32_16x16x32_bf16 v[10:13], v[192:195], v[224:227], v[10:13]
	s_setprio 0
	s_waitcnt vmcnt(8)
	s_barrier
	s_add_i32 s68, s68, 2
	s_add_u32 s50, s50, 0x100
	s_addc_u32 s51, s51, 0
	s_cmp_gt_u32 s68, 5
	s_cbranch_scc0 .LBB0_1025
	s_and_b64 vcc, exec, s[42:43]
	s_cbranch_vccz .LBB0_1028
	s_barrier

; #define PG8_STAGE(bufoff, gbase, voff) do { _Pragma("unroll") for (int _i = 0; _i < 2; ++_i) \
;         __builtin_amdgcn_global_load_lds((const unsigned*)((const char*)(gbase) + (voff)[_i]), (LAS unsigned*)(lds + (bufoff) + ldsw + _i * 8192), 16, 0, 0); } while (0)
; #define PG8_LDA(dst, b, h) do { if constexpr (FP8) { _Pragma("unroll") for (int m = 0; m < 4; ++m) dst##8[m] = PG8_LD8(lds + PG8_SA(b, h) + aoff + m * 2048); } \
;         else { _Pragma("unroll") for (int m = 0; m < 4; ++m) _Pragma("unroll") for (int k = 0; k < 2; ++k) dst[m][k] = *(const LAS bf16x8*)(lds + PG8_SA(b, h) + aoff + m * 2048 + k * 1024); } } while (0)
; #define PG8_LDB(dst, b, h) do { if constexpr (FP8) { _Pragma("unroll") for (int n = 0; n < 2; ++n) dst##8[n] = PG8_LD8(lds + PG8_SB(b, h) + boff + n * 2048); } \
;         else { _Pragma("unroll") for (int n = 0; n < 2; ++n) _Pragma("unroll") for (int k = 0; k < 2; ++k) dst[n][k] = *(const LAS bf16x8*)(lds + PG8_SB(b, h) + boff + n * 2048 + k * 1024); } } while (0)
; #define PG8_WAIT_V(n) asm volatile("s_waitcnt vmcnt(" #n ")" ::: "memory")
; #define PG8_WAIT_L(n) asm volatile("s_waitcnt lgkmcnt(" #n ")" ::: "memory")
; #define PG8_BAR __builtin_amdgcn_s_barrier()
; #define PG8_SCHED __builtin_amdgcn_sched_barrier(0)
; template <class Epi, class Sched, bool ALIGN_EPI, bool SP2, bool FP8 = false>
; __device__ __forceinline__ void gemm_phase(LAS unsigned char* lds, const int K, const Sched& S, const Epi& E) {
;     ...
;         for (int t = 0; t < nt; t += 2) {
;             const bool last = (t == nt - 2);
;             const char* a1 = cA + (size_t)(t + 1) * kstep;
;             const char* a2 = last ? nA : cA + (size_t)(t + 2) * kstep; const char* b2 = last ? nB : cB + (size_t)(t + 2) * kstep;
;             const char* a3 = a2 + kstep; const char* b3 = b2 + kstep;
;             unsigned vX0[2], vX1[2];
; #pragma unroll
;             for (int i = 0; i < 2; ++i) { vX0[i] = last ? vAn[0][i] : vAc[0][i]; vX1[i] = last ? vAn[1][i] : vAc[1][i]; }
;             PG8_LDB(B0, 0, 0); PG8_LDB(B1, 0, 1); PG8_SCHED; PG8_LDA(At, 0, 0); PG8_STAGE(PG8_SA(1, 1), a1, vAc[1]);
;             PG8_WAIT_V(8); PG8_WAIT_L(0); PG8_BAR; PG8_MMA(0, 0, At, B0); PG8_MMA(0, 1, At, B1); PG8_BAR; PG8_SCHED;
;             PG8_LDA(At, 0, 1); PG8_STAGE(PG8_SB(0, 0), b2, voffB); PG8_STAGE(PG8_SB(0, 1), b2 + hstep, voffB); PG8_STAGE(PG8_SA(0, 0), a2, vX0);
.LBB0_1189:
	s_add_u32 s49, s30, s50
	s_addc_u32 s56, s31, s51
	v_add_u32_e32 v2, s75, v193
	v_add_u32_e32 v14, s76, v193
	s_add_u32 s49, s49, 0x2c000100
	ds_read_b128 v[18:21], v2
	ds_read_b128 v[22:25], v2 offset:1024
	ds_read_b128 v[26:29], v2 offset:2048
	ds_read_b128 v[30:33], v2 offset:3072
	ds_read_b128 v[2:5], v14
	ds_read_b128 v[6:9], v14 offset:1024
	ds_read_b128 v[10:13], v14 offset:2048
	ds_read_b128 v[14:17], v14 offset:3072
	s_addc_u32 s58, s56, 0
	s_add_u32 s81, s43, s50
	s_addc_u32 s82, s45, s51
	s_cmpk_eq_i32 s50, 0x700
	s_cselect_b64 vcc, -1, 0
	s_and_b64 s[56:57], vcc, exec
	v_cndmask_b32_e32 v162, v211, v1, vcc
	s_cselect_b32 s59, s11, s58
	s_cselect_b32 s58, s10, s49
	v_cndmask_b32_e32 v171, v170, v189, vcc
	v_cndmask_b32_e32 v244, v174, v188, vcc
	v_cndmask_b32_e32 v173, v172, v191, vcc
	s_cselect_b32 s57, s41, s82
	s_cselect_b32 s56, s40, s81
	v_lshl_add_u64 v[236:237], v[178:179], 0, s[50:51]
	s_add_i32 m0, s64, 0xc000
	ds_read_b128 v[180:183], v204
	ds_read_b128 v[184:187], v204 offset:1024
	ds_read_b128 v[212:215], v204 offset:2048
	ds_read_b128 v[216:219], v204 offset:3072
	ds_read_b128 v[220:223], v204 offset:4096
	ds_read_b128 v[224:227], v204 offset:5120
	ds_read_b128 v[228:231], v204 offset:6144
	ds_read_b128 v[232:235], v204 offset:7168
	global_load_lds_dwordx4 v[236:237], off
	v_lshl_add_u64 v[236:237], v[176:177], 0, s[50:51]
	s_add_i32 m0, s64, 0xe000
	s_nop 0
	global_load_lds_dwordx4 v[236:237], off
	s_bitcmp1_b32 s38, 0
	s_cbranch_scc1 .Lg0skip_17
	s_waitcnt vmcnt(8)
.Lg0skip_17:
	s_waitcnt lgkmcnt(0)
	s_setprio 1
	s_barrier
	v_mfma_f32_16x16x128_f8f6f4 v[150:153], v[18:25], v[180:187], v[150:153]
	v_mfma_f32_16x16x128_f8f6f4 v[158:161], v[26:33], v[180:187], v[158:161]
	v_mfma_f32_16x16x128_f8f6f4 v[134:137], v[18:25], v[212:219], v[134:137]
	v_mfma_f32_16x16x128_f8f6f4 v[142:145], v[26:33], v[212:219], v[142:145]
	v_mfma_f32_16x16x128_f8f6f4 v[118:121], v[18:25], v[220:227], v[118:121]
	v_mfma_f32_16x16x128_f8f6f4 v[126:129], v[26:33], v[220:227], v[126:129]
	v_mfma_f32_16x16x128_f8f6f4 v[102:105], v[18:25], v[228:235], v[102:105]
	v_mfma_f32_16x16x128_f8f6f4 v[110:113], v[26:33], v[228:235], v[110:113]
	v_mfma_f32_16x16x128_f8f6f4 v[146:149], v[2:9], v[180:187], v[146:149]
	v_mfma_f32_16x16x128_f8f6f4 v[154:157], v[10:17], v[180:187], v[154:157]
	v_mfma_f32_16x16x128_f8f6f4 v[130:133], v[2:9], v[212:219], v[130:133]
	v_mfma_f32_16x16x128_f8f6f4 v[138:141], v[10:17], v[212:219], v[138:141]
	v_mfma_f32_16x16x128_f8f6f4 v[114:117], v[2:9], v[220:227], v[114:117]
	v_mfma_f32_16x16x128_f8f6f4 v[122:125], v[10:17], v[220:227], v[122:125]
	v_mfma_f32_16x16x128_f8f6f4 v[98:101], v[2:9], v[228:235], v[98:101]
	v_mfma_f32_16x16x128_f8f6f4 v[106:109], v[10:17], v[228:235], v[106:109]
	s_setprio 0
	s_waitcnt vmcnt(8)
	s_barrier
	s_add_i32 s49, s75, s63
	v_lshl_add_u64 v[180:181], s[56:57], 0, v[164:165]
	s_mov_b32 m0, s49
	ds_read_b128 v[212:215], v204 offset:16384
	ds_read_b128 v[216:219], v204 offset:17408
	ds_read_b128 v[220:223], v204 offset:18432
	ds_read_b128 v[224:227], v204 offset:19456
	ds_read_b128 v[228:231], v204 offset:20480
	ds_read_b128 v[232:235], v204 offset:21504
	ds_read_b128 v[236:239], v204 offset:22528
	ds_read_b128 v[240:243], v204 offset:23552
	global_load_lds_dwordx4 v[180:181], off
	s_add_i32 m0, s49, 0x2000
	s_add_u32 s82, s56, 0x40000
	v_lshl_add_u64 v[182:183], s[56:57], 0, v[166:167]
	s_addc_u32 s83, s57, 0
	s_add_i32 s49, s76, s63
	global_load_lds_dwordx4 v[182:183], off
	v_lshl_add_u64 v[184:185], s[82:83], 0, v[164:165]
	s_mov_b32 m0, s49
	v_mov_b32_e32 v245, v163
	global_load_lds_dwordx4 v[184:185], off
	v_lshl_add_u64 v[184:185], s[82:83], 0, v[166:167]
	s_add_i32 m0, s49, 0x2000
	v_lshl_add_u64 v[186:187], s[58:59], 0, v[162:163]
	global_load_lds_dwordx4 v[184:185], off
	s_mov_b32 m0, s64
	v_lshl_add_u64 v[184:185], s[58:59], 0, v[244:245]
	global_load_lds_dwordx4 v162, s[58:59]
	s_mov_b32 m0, s65
	s_nop 0
	global_load_lds_dwordx4 v244, s[58:59]
	s_bitcmp1_b32 s38, 0
	s_cbranch_scc1 .Lg0skip_18
	s_waitcnt vmcnt(8)
; #define PG8_STAGE(bufoff, gbase, voff) do { _Pragma("unroll") for (int _i = 0; _i < 2; ++_i) \
;         __builtin_amdgcn_global_load_lds((const unsigned*)((const char*)(gbase) + (voff)[_i]), (LAS unsigned*)(lds + (bufoff) + ldsw + _i * 8192), 16, 0, 0); } while (0)
; #define PG8_LDA(dst, b, h) do { if constexpr (FP8) { _Pragma("unroll") for (int m = 0; m < 4; ++m) dst##8[m] = PG8_LD8(lds + PG8_SA(b, h) + aoff + m * 2048); } \
;         else { _Pragma("unroll") for (int m = 0; m < 4; ++m) _Pragma("unroll") for (int k = 0; k < 2; ++k) dst[m][k] = *(const LAS bf16x8*)(lds + PG8_SA(b, h) + aoff + m * 2048 + k * 1024); } } while (0)
; #define PG8_LDB(dst, b, h) do { if constexpr (FP8) { _Pragma("unroll") for (int n = 0; n < 2; ++n) dst##8[n] = PG8_LD8(lds + PG8_SB(b, h) + boff + n * 2048); } \
;         else { _Pragma("unroll") for (int n = 0; n < 2; ++n) _Pragma("unroll") for (int k = 0; k < 2; ++k) dst[n][k] = *(const LAS bf16x8*)(lds + PG8_SB(b, h) + boff + n * 2048 + k * 1024); } } while (0)
; #define PG8_WAIT_V(n) asm volatile("s_waitcnt vmcnt(" #n ")" ::: "memory")
; #define PG8_WAIT_L(n) asm volatile("s_waitcnt lgkmcnt(" #n ")" ::: "memory")
; #define PG8_BAR __builtin_amdgcn_s_barrier()
; #define PG8_SCHED __builtin_amdgcn_sched_barrier(0)
; template <class Epi, class Sched, bool ALIGN_EPI, bool SP2, bool FP8 = false>
; __device__ __forceinline__ void gemm_phase(LAS unsigned char* lds, const int K, const Sched& S, const Epi& E) {
;     ...
;             PG8_WAIT_V(8); PG8_WAIT_L(0); PG8_BAR; PG8_MMA(1, 0, At, B0); PG8_MMA(1, 1, At, B1); PG8_BAR; PG8_SCHED;
;             PG8_LDB(B0, 1, 0); PG8_LDB(B1, 1, 1); PG8_SCHED; PG8_LDA(At, 1, 0); PG8_STAGE(PG8_SA(0, 1), a2, vX1);
;             PG8_WAIT_V(8); PG8_WAIT_L(0); PG8_BAR; PG8_MMA(0, 0, At, B0); PG8_MMA(0, 1, At, B1); PG8_BAR; PG8_SCHED;
;             PG8_LDA(At, 1, 1); PG8_STAGE(PG8_SB(1, 0), b3, voffB); PG8_STAGE(PG8_SB(1, 1), b3 + hstep, voffB); PG8_STAGE(PG8_SA(1, 0), a3, vX0);
;             PG8_WAIT_V(8); PG8_WAIT_L(0); PG8_BAR; PG8_MMA(1, 0, At, B0); PG8_MMA(1, 1, At, B1); PG8_BAR; PG8_SCHED;
;         }
;         if constexpr (ALIGN_EPI) { if (wr == 0) PG8_BAR; }
.Lg0skip_18:
	s_waitcnt lgkmcnt(0)
	s_setprio 1
	s_barrier
	v_mfma_f32_16x16x128_f8f6f4 v[86:89], v[18:25], v[212:219], v[86:89]
	v_mfma_f32_16x16x128_f8f6f4 v[94:97], v[26:33], v[212:219], v[94:97]
	v_mfma_f32_16x16x128_f8f6f4 v[66:69], v[18:25], v[220:227], v[66:69]
	v_mfma_f32_16x16x128_f8f6f4 v[78:81], v[26:33], v[220:227], v[78:81]
	v_mfma_f32_16x16x128_f8f6f4 v[46:49], v[18:25], v[228:235], v[46:49]
	v_mfma_f32_16x16x128_f8f6f4 v[54:57], v[26:33], v[228:235], v[54:57]
	v_mfma_f32_16x16x128_f8f6f4 v[34:37], v[18:25], v[236:243], v[34:37]
	v_mfma_f32_16x16x128_f8f6f4 v[38:41], v[26:33], v[236:243], v[38:41]
	v_mfma_f32_16x16x128_f8f6f4 v[82:85], v[2:9], v[212:219], v[82:85]
	v_mfma_f32_16x16x128_f8f6f4 v[90:93], v[10:17], v[212:219], v[90:93]
	v_mfma_f32_16x16x128_f8f6f4 v[62:65], v[2:9], v[220:227], v[62:65]
	v_mfma_f32_16x16x128_f8f6f4 v[74:77], v[10:17], v[220:227], v[74:77]
	v_mfma_f32_16x16x128_f8f6f4 v[58:61], v[2:9], v[228:235], v[58:61]
	v_mfma_f32_16x16x128_f8f6f4 v[70:73], v[10:17], v[228:235], v[70:73]
	v_mfma_f32_16x16x128_f8f6f4 v[42:45], v[2:9], v[236:243], v[42:45]
	v_mfma_f32_16x16x128_f8f6f4 v[50:53], v[10:17], v[236:243], v[50:53]
	s_setprio 0
	s_waitcnt vmcnt(8)
	s_barrier
	s_add_i32 s49, 0, 0x18000
	s_add_i32 s81, 0, 0x1c000
	v_add_u32_e32 v14, s49, v193
	v_add_u32_e32 v30, s81, v193
	ds_read_b128 v[2:5], v14
	ds_read_b128 v[6:9], v14 offset:1024
	ds_read_b128 v[10:13], v14 offset:2048
	ds_read_b128 v[14:17], v14 offset:3072
	ds_read_b128 v[18:21], v30
	ds_read_b128 v[22:25], v30 offset:1024
	ds_read_b128 v[26:29], v30 offset:2048
	ds_read_b128 v[30:33], v30 offset:3072
	s_mov_b32 m0, s66
	ds_read_b128 v[212:215], v204 offset:32768
	ds_read_b128 v[216:219], v204 offset:33792
	ds_read_b128 v[220:223], v204 offset:34816
	ds_read_b128 v[224:227], v204 offset:35840
	ds_read_b128 v[228:231], v204 offset:36864
	ds_read_b128 v[232:235], v204 offset:37888
	ds_read_b128 v[236:239], v204 offset:38912
	ds_read_b128 v[240:243], v204 offset:39936
	global_load_lds_dwordx4 v171, s[58:59]
	s_mov_b32 m0, s67
	s_nop 0
	global_load_lds_dwordx4 v173, s[58:59]
	s_bitcmp1_b32 s38, 0
	s_cbranch_scc1 .Lg0skip_19
	s_waitcnt vmcnt(8)
.Lg0skip_19:
	s_waitcnt lgkmcnt(0)
	s_setprio 1
	s_barrier
	v_mfma_f32_16x16x128_f8f6f4 v[150:153], v[2:9], v[212:219], v[150:153]
	v_mfma_f32_16x16x128_f8f6f4 v[158:161], v[10:17], v[212:219], v[158:161]
	v_mfma_f32_16x16x128_f8f6f4 v[134:137], v[2:9], v[220:227], v[134:137]
	v_mfma_f32_16x16x128_f8f6f4 v[142:145], v[10:17], v[220:227], v[142:145]
	v_mfma_f32_16x16x128_f8f6f4 v[118:121], v[2:9], v[228:235], v[118:121]
	v_mfma_f32_16x16x128_f8f6f4 v[126:129], v[10:17], v[228:235], v[126:129]
	v_mfma_f32_16x16x128_f8f6f4 v[102:105], v[2:9], v[236:243], v[102:105]
	v_mfma_f32_16x16x128_f8f6f4 v[110:113], v[10:17], v[236:243], v[110:113]
	v_mfma_f32_16x16x128_f8f6f4 v[146:149], v[18:25], v[212:219], v[146:149]
	v_mfma_f32_16x16x128_f8f6f4 v[154:157], v[26:33], v[212:219], v[154:157]
	v_mfma_f32_16x16x128_f8f6f4 v[130:133], v[18:25], v[220:227], v[130:133]
	v_mfma_f32_16x16x128_f8f6f4 v[138:141], v[26:33], v[220:227], v[138:141]
	v_mfma_f32_16x16x128_f8f6f4 v[114:117], v[18:25], v[228:235], v[114:117]
	v_mfma_f32_16x16x128_f8f6f4 v[122:125], v[26:33], v[228:235], v[122:125]
	v_mfma_f32_16x16x128_f8f6f4 v[98:101], v[18:25], v[236:243], v[98:101]
	v_mfma_f32_16x16x128_f8f6f4 v[106:109], v[26:33], v[236:243], v[106:109]
	s_setprio 0
	s_waitcnt vmcnt(8)
	s_barrier
	s_add_i32 s49, s49, s63
	v_lshl_add_u64 v[180:181], v[180:181], 0, s[16:17]
	s_mov_b32 m0, s49
	ds_read_b128 v[212:215], v204 offset:49152
	ds_read_b128 v[216:219], v204 offset:50176
	ds_read_b128 v[220:223], v204 offset:51200
	ds_read_b128 v[224:227], v204 offset:52224
	ds_read_b128 v[228:231], v204 offset:53248
	ds_read_b128 v[232:235], v204 offset:54272
	ds_read_b128 v[236:239], v204 offset:55296
	ds_read_b128 v[240:243], v204 offset:56320
	global_load_lds_dwordx4 v[180:181], off
	s_add_i32 m0, s49, 0x2000
	s_add_u32 s56, s56, 0x40080
	v_lshl_add_u64 v[180:181], v[182:183], 0, s[16:17]
	s_addc_u32 s57, s57, 0
	s_add_i32 s49, s81, s63
	global_load_lds_dwordx4 v[180:181], off
	v_lshl_add_u64 v[180:181], s[56:57], 0, v[164:165]
	s_mov_b32 m0, s49
	s_nop 0
	global_load_lds_dwordx4 v[180:181], off
	v_lshl_add_u64 v[180:181], s[56:57], 0, v[166:167]
	s_add_i32 m0, s49, 0x2000
	s_nop 0
	global_load_lds_dwordx4 v[180:181], off
	v_lshl_add_u64 v[180:181], v[186:187], 0, s[16:17]
	s_mov_b32 m0, s70
	s_nop 0
	global_load_lds_dwordx4 v[180:181], off
	v_lshl_add_u64 v[180:181], v[184:185], 0, s[16:17]
	s_mov_b32 m0, s71
	s_nop 0
	global_load_lds_dwordx4 v[180:181], off
	s_bitcmp1_b32 s38, 0
	s_cbranch_scc1 .Lg0skip_20
	s_waitcnt vmcnt(8)
.Lg0skip_20:
	s_waitcnt lgkmcnt(0)
	s_setprio 1
	s_barrier
	v_mfma_f32_16x16x128_f8f6f4 v[86:89], v[2:9], v[212:219], v[86:89]
	v_mfma_f32_16x16x128_f8f6f4 v[94:97], v[10:17], v[212:219], v[94:97]
	v_mfma_f32_16x16x128_f8f6f4 v[66:69], v[2:9], v[220:227], v[66:69]
	v_mfma_f32_16x16x128_f8f6f4 v[78:81], v[10:17], v[220:227], v[78:81]
	v_mfma_f32_16x16x128_f8f6f4 v[46:49], v[2:9], v[228:235], v[46:49]
	v_mfma_f32_16x16x128_f8f6f4 v[54:57], v[10:17], v[228:235], v[54:57]
	v_mfma_f32_16x16x128_f8f6f4 v[34:37], v[2:9], v[236:243], v[34:37]
	v_mfma_f32_16x16x128_f8f6f4 v[38:41], v[10:17], v[236:243], v[38:41]
	v_mfma_f32_16x16x128_f8f6f4 v[82:85], v[18:25], v[212:219], v[82:85]
	v_mfma_f32_16x16x128_f8f6f4 v[90:93], v[26:33], v[212:219], v[90:93]
	v_mfma_f32_16x16x128_f8f6f4 v[62:65], v[18:25], v[220:227], v[62:65]
	v_mfma_f32_16x16x128_f8f6f4 v[74:77], v[26:33], v[220:227], v[74:77]
	v_mfma_f32_16x16x128_f8f6f4 v[58:61], v[18:25], v[228:235], v[58:61]
	v_mfma_f32_16x16x128_f8f6f4 v[70:73], v[26:33], v[228:235], v[70:73]
	v_mfma_f32_16x16x128_f8f6f4 v[42:45], v[18:25], v[236:243], v[42:45]
	v_mfma_f32_16x16x128_f8f6f4 v[50:53], v[26:33], v[236:243], v[50:53]
	s_setprio 0
	s_waitcnt vmcnt(8)
	s_barrier
	s_add_i32 s47, s47, 2
	s_add_u32 s50, s50, 0x100
	s_addc_u32 s51, s51, 0
	s_cmp_gt_u32 s47, 13
	s_cbranch_scc0 .LBB0_1189
	s_and_b64 vcc, exec, s[38:39]
	s_cbranch_vccz .LBB0_1192
	s_barrier

; #define PG8_STAGE(bufoff, gbase, voff) do { _Pragma("unroll") for (int _i = 0; _i < 2; ++_i) \
;         __builtin_amdgcn_global_load_lds((const unsigned*)((const char*)(gbase) + (voff)[_i]), (LAS unsigned*)(lds + (bufoff) + ldsw + _i * 8192), 16, 0, 0); } while (0)
; #define PG8_LDA(dst, b, h) do { if constexpr (FP8) { _Pragma("unroll") for (int m = 0; m < 4; ++m) dst##8[m] = PG8_LD8(lds + PG8_SA(b, h) + aoff + m * 2048); } \
;         else { _Pragma("unroll") for (int m = 0; m < 4; ++m) _Pragma("unroll") for (int k = 0; k < 2; ++k) dst[m][k] = *(const LAS bf16x8*)(lds + PG8_SA(b, h) + aoff + m * 2048 + k * 1024); } } while (0)
; #define PG8_LDB(dst, b, h) do { if constexpr (FP8) { _Pragma("unroll") for (int n = 0; n < 2; ++n) dst##8[n] = PG8_LD8(lds + PG8_SB(b, h) + boff + n * 2048); } \
;         else { _Pragma("unroll") for (int n = 0; n < 2; ++n) _Pragma("unroll") for (int k = 0; k < 2; ++k) dst[n][k] = *(const LAS bf16x8*)(lds + PG8_SB(b, h) + boff + n * 2048 + k * 1024); } } while (0)
; #define PG8_WAIT_V(n) asm volatile("s_waitcnt vmcnt(" #n ")" ::: "memory")
; #define PG8_WAIT_L(n) asm volatile("s_waitcnt lgkmcnt(" #n ")" ::: "memory")
; #define PG8_BAR __builtin_amdgcn_s_barrier()
; #define PG8_SCHED __builtin_amdgcn_sched_barrier(0)
; template <class Epi, class Sched, bool ALIGN_EPI, bool SP2, bool FP8 = false>
; __device__ __forceinline__ void gemm_phase(LAS unsigned char* lds, const int K, const Sched& S, const Epi& E) {
;     ...
;         for (int t = 0; t < nt; t += 2) {
;             const bool last = (t == nt - 2);
;             const char* a1 = cA + (size_t)(t + 1) * kstep;
;             const char* a2 = last ? nA : cA + (size_t)(t + 2) * kstep; const char* b2 = last ? nB : cB + (size_t)(t + 2) * kstep;
;             const char* a3 = a2 + kstep; const char* b3 = b2 + kstep;
;             unsigned vX0[2], vX1[2];
; #pragma unroll
;             for (int i = 0; i < 2; ++i) { vX0[i] = last ? vAn[0][i] : vAc[0][i]; vX1[i] = last ? vAn[1][i] : vAc[1][i]; }
;             PG8_LDB(B0, 0, 0); PG8_LDB(B1, 0, 1); PG8_SCHED; PG8_LDA(At, 0, 0); PG8_STAGE(PG8_SA(1, 1), a1, vAc[1]);
;             PG8_WAIT_V(8); PG8_WAIT_L(0); PG8_BAR; PG8_MMA(0, 0, At, B0); PG8_MMA(0, 1, At, B1); PG8_BAR; PG8_SCHED;
;             PG8_LDA(At, 0, 1); PG8_STAGE(PG8_SB(0, 0), b2, voffB); PG8_STAGE(PG8_SB(0, 1), b2 + hstep, voffB); PG8_STAGE(PG8_SA(0, 0), a2, vX0);
.LBB0_1329:
	s_add_u32 s56, s30, s50
	s_addc_u32 s57, s31, s51
	s_add_u32 s58, s56, 0x60000100
	s_addc_u32 s59, s57, 0
	s_add_u32 s81, s41, s50
	s_addc_u32 s82, s43, s51
	s_cmpk_eq_i32 s50, 0x700
	s_cselect_b64 vcc, -1, 0
	s_and_b64 s[56:57], vcc, exec
	s_cselect_b32 s59, s9, s59
	s_cselect_b32 s58, s8, s58
	s_cselect_b32 s57, s45, s82
	s_cselect_b32 s56, s44, s81
	s_add_i32 s81, 0, 0x10000
	s_add_i32 s82, 0, 0x14000
	v_add_u32_e32 v2, s81, v196
	v_add_u32_e32 v14, s82, v196
	ds_read_b128 v[18:21], v2
	ds_read_b128 v[22:25], v2 offset:1024
	ds_read_b128 v[26:29], v2 offset:2048
	ds_read_b128 v[30:33], v2 offset:3072
	ds_read_b128 v[2:5], v14
	ds_read_b128 v[6:9], v14 offset:1024
	ds_read_b128 v[10:13], v14 offset:2048
	ds_read_b128 v[14:17], v14 offset:3072
	v_cndmask_b32_e32 v166, v172, v204, vcc
	v_cndmask_b32_e32 v171, v170, v205, vcc
	v_cndmask_b32_e32 v240, v176, v206, vcc
	v_cndmask_b32_e32 v175, v174, v207, vcc
	v_lshl_add_u64 v[232:233], v[180:181], 0, s[50:51]
	s_add_i32 m0, s71, 0xc000
	ds_read_b128 v[182:185], v203
	ds_read_b128 v[186:189], v203 offset:1024
	ds_read_b128 v[208:211], v203 offset:2048
	ds_read_b128 v[212:215], v203 offset:3072
	ds_read_b128 v[216:219], v203 offset:4096
	ds_read_b128 v[220:223], v203 offset:5120
	ds_read_b128 v[224:227], v203 offset:6144
	ds_read_b128 v[228:231], v203 offset:7168
	global_load_lds_dwordx4 v[232:233], off
	v_lshl_add_u64 v[232:233], v[178:179], 0, s[50:51]
	s_add_i32 m0, s71, 0xe000
	s_nop 0
	global_load_lds_dwordx4 v[232:233], off
	s_bitcmp1_b32 s38, 0
	s_cbranch_scc1 .Lg0skip_21
	s_waitcnt vmcnt(8)
.Lg0skip_21:
	s_waitcnt lgkmcnt(0)
	s_setprio 1
	s_barrier
	v_mfma_f32_16x16x128_f8f6f4 v[158:161], v[18:25], v[182:189], v[158:161]
	v_mfma_f32_16x16x128_f8f6f4 v[154:157], v[26:33], v[182:189], v[154:157]
	v_mfma_f32_16x16x128_f8f6f4 v[142:145], v[18:25], v[208:215], v[142:145]
	v_mfma_f32_16x16x128_f8f6f4 v[138:141], v[26:33], v[208:215], v[138:141]
	v_mfma_f32_16x16x128_f8f6f4 v[126:129], v[18:25], v[216:223], v[126:129]
	v_mfma_f32_16x16x128_f8f6f4 v[122:125], v[26:33], v[216:223], v[122:125]
	v_mfma_f32_16x16x128_f8f6f4 v[110:113], v[18:25], v[224:231], v[110:113]
	v_mfma_f32_16x16x128_f8f6f4 v[106:109], v[26:33], v[224:231], v[106:109]
	v_mfma_f32_16x16x128_f8f6f4 v[150:153], v[2:9], v[182:189], v[150:153]
	v_mfma_f32_16x16x128_f8f6f4 v[146:149], v[10:17], v[182:189], v[146:149]
	v_mfma_f32_16x16x128_f8f6f4 v[134:137], v[2:9], v[208:215], v[134:137]
	v_mfma_f32_16x16x128_f8f6f4 v[130:133], v[10:17], v[208:215], v[130:133]
	v_mfma_f32_16x16x128_f8f6f4 v[118:121], v[2:9], v[216:223], v[118:121]
	v_mfma_f32_16x16x128_f8f6f4 v[114:117], v[10:17], v[216:223], v[114:117]
	v_mfma_f32_16x16x128_f8f6f4 v[102:105], v[2:9], v[224:231], v[102:105]
	v_mfma_f32_16x16x128_f8f6f4 v[98:101], v[10:17], v[224:231], v[98:101]
	s_setprio 0
	s_waitcnt vmcnt(8)
	s_barrier
	s_add_i32 s81, s81, s70
	v_lshl_add_u64 v[182:183], s[56:57], 0, v[162:163]
	s_mov_b32 m0, s81
	ds_read_b128 v[208:211], v203 offset:16384
	ds_read_b128 v[212:215], v203 offset:17408
	ds_read_b128 v[216:219], v203 offset:18432
	ds_read_b128 v[220:223], v203 offset:19456
	ds_read_b128 v[224:227], v203 offset:20480
	ds_read_b128 v[228:231], v203 offset:21504
	ds_read_b128 v[232:235], v203 offset:22528
	ds_read_b128 v[236:239], v203 offset:23552
	global_load_lds_dwordx4 v[182:183], off
	s_add_i32 m0, s81, 0x2000
	s_add_u32 s84, s56, 0x40000
	v_lshl_add_u64 v[184:185], s[56:57], 0, v[164:165]
	s_addc_u32 s85, s57, 0
	s_add_i32 s81, s82, s70
	global_load_lds_dwordx4 v[184:185], off
	v_lshl_add_u64 v[186:187], s[84:85], 0, v[162:163]
	s_mov_b32 m0, s81
	v_mov_b32_e32 v241, v167
	global_load_lds_dwordx4 v[186:187], off
	v_lshl_add_u64 v[186:187], s[84:85], 0, v[164:165]
	s_add_i32 m0, s81, 0x2000
	v_lshl_add_u64 v[188:189], s[58:59], 0, v[166:167]
	global_load_lds_dwordx4 v[186:187], off
	s_mov_b32 m0, s71
	v_lshl_add_u64 v[186:187], s[58:59], 0, v[240:241]
	global_load_lds_dwordx4 v166, s[58:59]
	s_mov_b32 m0, s72
	s_nop 0
	global_load_lds_dwordx4 v240, s[58:59]
	s_bitcmp1_b32 s38, 0
	s_cbranch_scc1 .Lg0skip_22
	s_waitcnt vmcnt(8)
; #define PG8_STAGE(bufoff, gbase, voff) do { _Pragma("unroll") for (int _i = 0; _i < 2; ++_i) \
;         __builtin_amdgcn_global_load_lds((const unsigned*)((const char*)(gbase) + (voff)[_i]), (LAS unsigned*)(lds + (bufoff) + ldsw + _i * 8192), 16, 0, 0); } while (0)
; #define PG8_LDA(dst, b, h) do { if constexpr (FP8) { _Pragma("unroll") for (int m = 0; m < 4; ++m) dst##8[m] = PG8_LD8(lds + PG8_SA(b, h) + aoff + m * 2048); } \
;         else { _Pragma("unroll") for (int m = 0; m < 4; ++m) _Pragma("unroll") for (int k = 0; k < 2; ++k) dst[m][k] = *(const LAS bf16x8*)(lds + PG8_SA(b, h) + aoff + m * 2048 + k * 1024); } } while (0)
; #define PG8_LDB(dst, b, h) do { if constexpr (FP8) { _Pragma("unroll") for (int n = 0; n < 2; ++n) dst##8[n] = PG8_LD8(lds + PG8_SB(b, h) + boff + n * 2048); } \
;         else { _Pragma("unroll") for (int n = 0; n < 2; ++n) _Pragma("unroll") for (int k = 0; k < 2; ++k) dst[n][k] = *(const LAS bf16x8*)(lds + PG8_SB(b, h) + boff + n * 2048 + k * 1024); } } while (0)
; #define PG8_WAIT_V(n) asm volatile("s_waitcnt vmcnt(" #n ")" ::: "memory")
; #define PG8_WAIT_L(n) asm volatile("s_waitcnt lgkmcnt(" #n ")" ::: "memory")
; #define PG8_BAR __builtin_amdgcn_s_barrier()
; #define PG8_SCHED __builtin_amdgcn_sched_barrier(0)
; template <class Epi, class Sched, bool ALIGN_EPI, bool SP2, bool FP8 = false>
; __device__ __forceinline__ void gemm_phase(LAS unsigned char* lds, const int K, const Sched& S, const Epi& E) {
;     ...
;             PG8_WAIT_V(8); PG8_WAIT_L(0); PG8_BAR; PG8_MMA(1, 0, At, B0); PG8_MMA(1, 1, At, B1); PG8_BAR; PG8_SCHED;
;             PG8_LDB(B0, 1, 0); PG8_LDB(B1, 1, 1); PG8_SCHED; PG8_LDA(At, 1, 0); PG8_STAGE(PG8_SA(0, 1), a2, vX1);
;             PG8_WAIT_V(8); PG8_WAIT_L(0); PG8_BAR; PG8_MMA(0, 0, At, B0); PG8_MMA(0, 1, At, B1); PG8_BAR; PG8_SCHED;
;             PG8_LDA(At, 1, 1); PG8_STAGE(PG8_SB(1, 0), b3, voffB); PG8_STAGE(PG8_SB(1, 1), b3 + hstep, voffB); PG8_STAGE(PG8_SA(1, 0), a3, vX0);
;             PG8_WAIT_V(8); PG8_WAIT_L(0); PG8_BAR; PG8_MMA(1, 0, At, B0); PG8_MMA(1, 1, At, B1); PG8_BAR; PG8_SCHED;
;         }
;         if constexpr (ALIGN_EPI) { if (wr == 0) PG8_BAR; }
.Lg0skip_22:
	s_waitcnt lgkmcnt(0)
	s_setprio 1
	s_barrier
	v_mfma_f32_16x16x128_f8f6f4 v[94:97], v[18:25], v[208:215], v[94:97]
	v_mfma_f32_16x16x128_f8f6f4 v[90:93], v[26:33], v[208:215], v[90:93]
	v_mfma_f32_16x16x128_f8f6f4 v[78:81], v[18:25], v[216:223], v[78:81]
	v_mfma_f32_16x16x128_f8f6f4 v[74:77], v[26:33], v[216:223], v[74:77]
	v_mfma_f32_16x16x128_f8f6f4 v[58:61], v[18:25], v[224:231], v[58:61]
	v_mfma_f32_16x16x128_f8f6f4 v[46:49], v[26:33], v[224:231], v[46:49]
	v_mfma_f32_16x16x128_f8f6f4 v[38:41], v[18:25], v[232:239], v[38:41]
	v_mfma_f32_16x16x128_f8f6f4 v[34:37], v[26:33], v[232:239], v[34:37]
	v_mfma_f32_16x16x128_f8f6f4 v[86:89], v[2:9], v[208:215], v[86:89]
	v_mfma_f32_16x16x128_f8f6f4 v[82:85], v[10:17], v[208:215], v[82:85]
	v_mfma_f32_16x16x128_f8f6f4 v[62:65], v[2:9], v[216:223], v[62:65]
	v_mfma_f32_16x16x128_f8f6f4 v[54:57], v[10:17], v[216:223], v[54:57]
	v_mfma_f32_16x16x128_f8f6f4 v[70:73], v[2:9], v[224:231], v[70:73]
	v_mfma_f32_16x16x128_f8f6f4 v[66:69], v[10:17], v[224:231], v[66:69]
	v_mfma_f32_16x16x128_f8f6f4 v[50:53], v[2:9], v[232:239], v[50:53]
	v_mfma_f32_16x16x128_f8f6f4 v[42:45], v[10:17], v[232:239], v[42:45]
	s_setprio 0
	s_waitcnt vmcnt(8)
	s_barrier
	s_add_i32 s81, 0, 0x18000
	s_add_i32 s82, 0, 0x1c000
	v_add_u32_e32 v14, s81, v196
	v_add_u32_e32 v30, s82, v196
	ds_read_b128 v[2:5], v14
	ds_read_b128 v[6:9], v14 offset:1024
	ds_read_b128 v[10:13], v14 offset:2048
	ds_read_b128 v[14:17], v14 offset:3072
	ds_read_b128 v[18:21], v30
	ds_read_b128 v[22:25], v30 offset:1024
	ds_read_b128 v[26:29], v30 offset:2048
	ds_read_b128 v[30:33], v30 offset:3072
	s_mov_b32 m0, s73
	ds_read_b128 v[208:211], v203 offset:32768
	ds_read_b128 v[212:215], v203 offset:33792
	ds_read_b128 v[216:219], v203 offset:34816
	ds_read_b128 v[220:223], v203 offset:35840
	ds_read_b128 v[224:227], v203 offset:36864
	ds_read_b128 v[228:231], v203 offset:37888
	ds_read_b128 v[232:235], v203 offset:38912
	ds_read_b128 v[236:239], v203 offset:39936
	global_load_lds_dwordx4 v171, s[58:59]
	s_mov_b32 m0, s74
	s_nop 0
	global_load_lds_dwordx4 v175, s[58:59]
	s_bitcmp1_b32 s38, 0
	s_cbranch_scc1 .Lg0skip_23
	s_waitcnt vmcnt(8)
.Lg0skip_23:
	s_waitcnt lgkmcnt(0)
	s_setprio 1
	s_barrier
	v_mfma_f32_16x16x128_f8f6f4 v[158:161], v[2:9], v[208:215], v[158:161]
	v_mfma_f32_16x16x128_f8f6f4 v[154:157], v[10:17], v[208:215], v[154:157]
	v_mfma_f32_16x16x128_f8f6f4 v[142:145], v[2:9], v[216:223], v[142:145]
	v_mfma_f32_16x16x128_f8f6f4 v[138:141], v[10:17], v[216:223], v[138:141]
	v_mfma_f32_16x16x128_f8f6f4 v[126:129], v[2:9], v[224:231], v[126:129]
	v_mfma_f32_16x16x128_f8f6f4 v[122:125], v[10:17], v[224:231], v[122:125]
	v_mfma_f32_16x16x128_f8f6f4 v[110:113], v[2:9], v[232:239], v[110:113]
	v_mfma_f32_16x16x128_f8f6f4 v[106:109], v[10:17], v[232:239], v[106:109]
	v_mfma_f32_16x16x128_f8f6f4 v[150:153], v[18:25], v[208:215], v[150:153]
	v_mfma_f32_16x16x128_f8f6f4 v[146:149], v[26:33], v[208:215], v[146:149]
	v_mfma_f32_16x16x128_f8f6f4 v[134:137], v[18:25], v[216:223], v[134:137]
	v_mfma_f32_16x16x128_f8f6f4 v[130:133], v[26:33], v[216:223], v[130:133]
	v_mfma_f32_16x16x128_f8f6f4 v[118:121], v[18:25], v[224:231], v[118:121]
	v_mfma_f32_16x16x128_f8f6f4 v[114:117], v[26:33], v[224:231], v[114:117]
	v_mfma_f32_16x16x128_f8f6f4 v[102:105], v[18:25], v[232:239], v[102:105]
	v_mfma_f32_16x16x128_f8f6f4 v[98:101], v[26:33], v[232:239], v[98:101]
	s_setprio 0
	s_waitcnt vmcnt(8)
	s_barrier
	s_add_i32 s58, s81, s70
	v_lshl_add_u64 v[182:183], v[182:183], 0, s[18:19]
	s_mov_b32 m0, s58
	ds_read_b128 v[208:211], v203 offset:49152
	ds_read_b128 v[212:215], v203 offset:50176
	ds_read_b128 v[216:219], v203 offset:51200
	ds_read_b128 v[220:223], v203 offset:52224
	ds_read_b128 v[224:227], v203 offset:53248
	ds_read_b128 v[228:231], v203 offset:54272
	ds_read_b128 v[232:235], v203 offset:55296
	ds_read_b128 v[236:239], v203 offset:56320
	global_load_lds_dwordx4 v[182:183], off
	s_add_i32 m0, s58, 0x2000
	s_add_u32 s56, s56, 0x40080
	v_lshl_add_u64 v[182:183], v[184:185], 0, s[18:19]
	s_addc_u32 s57, s57, 0
	s_add_i32 s58, s82, s70
	global_load_lds_dwordx4 v[182:183], off
	v_lshl_add_u64 v[182:183], s[56:57], 0, v[162:163]
	s_mov_b32 m0, s58
	s_nop 0
	global_load_lds_dwordx4 v[182:183], off
	v_lshl_add_u64 v[182:183], s[56:57], 0, v[164:165]
	s_add_i32 m0, s58, 0x2000
	s_nop 0
	global_load_lds_dwordx4 v[182:183], off
	v_lshl_add_u64 v[182:183], v[188:189], 0, s[18:19]
	s_mov_b32 m0, s75
	s_nop 0
	global_load_lds_dwordx4 v[182:183], off
	v_lshl_add_u64 v[182:183], v[186:187], 0, s[18:19]
	s_mov_b32 m0, s76
	s_nop 0
	global_load_lds_dwordx4 v[182:183], off
	s_bitcmp1_b32 s38, 0
	s_cbranch_scc1 .Lg0skip_24
	s_waitcnt vmcnt(8)
.Lg0skip_24:
	s_waitcnt lgkmcnt(0)
	s_setprio 1
	s_barrier
	v_mfma_f32_16x16x128_f8f6f4 v[94:97], v[2:9], v[208:215], v[94:97]
	v_mfma_f32_16x16x128_f8f6f4 v[90:93], v[10:17], v[208:215], v[90:93]
	v_mfma_f32_16x16x128_f8f6f4 v[78:81], v[2:9], v[216:223], v[78:81]
	v_mfma_f32_16x16x128_f8f6f4 v[74:77], v[10:17], v[216:223], v[74:77]
	v_mfma_f32_16x16x128_f8f6f4 v[58:61], v[2:9], v[224:231], v[58:61]
	v_mfma_f32_16x16x128_f8f6f4 v[46:49], v[10:17], v[224:231], v[46:49]
	v_mfma_f32_16x16x128_f8f6f4 v[38:41], v[2:9], v[232:239], v[38:41]
	v_mfma_f32_16x16x128_f8f6f4 v[34:37], v[10:17], v[232:239], v[34:37]
	v_mfma_f32_16x16x128_f8f6f4 v[86:89], v[18:25], v[208:215], v[86:89]
	v_mfma_f32_16x16x128_f8f6f4 v[82:85], v[26:33], v[208:215], v[82:85]
	v_mfma_f32_16x16x128_f8f6f4 v[62:65], v[18:25], v[216:223], v[62:65]
	v_mfma_f32_16x16x128_f8f6f4 v[54:57], v[26:33], v[216:223], v[54:57]
	v_mfma_f32_16x16x128_f8f6f4 v[70:73], v[18:25], v[224:231], v[70:73]
	v_mfma_f32_16x16x128_f8f6f4 v[66:69], v[26:33], v[224:231], v[66:69]
	v_mfma_f32_16x16x128_f8f6f4 v[50:53], v[18:25], v[232:239], v[50:53]
	v_mfma_f32_16x16x128_f8f6f4 v[42:45], v[26:33], v[232:239], v[42:45]
	s_setprio 0
	s_waitcnt vmcnt(8)
	s_barrier
	s_add_i32 s49, s49, 2
	s_add_u32 s50, s50, 0x100
	s_addc_u32 s51, s51, 0
	s_cmp_gt_u32 s49, 13
	s_cbranch_scc0 .LBB0_1329
	s_and_b64 vcc, exec, s[38:39]
	s_cbranch_vccz .LBB0_1332
	s_barrier
